# baseline (speedup 1.0000x reference)
_Z7kf_mainPKfPKiPfPjS3_S4_:
	s_ashr_i32 s24, s2, 7
	s_load_dwordx4 s[4:7], s[0:1], 0x0
	s_ashr_i32 s9, s2, 3
	s_mul_i32 s8, s24, 5
	s_and_b32 s3, s9, 15
	s_ashr_i32 s10, s8, 31
	s_lshl_b32 s8, s8, 4
	s_or_b32 s8, s8, s3
	s_mul_hi_u32 s11, s8, 0xc8000
	s_mul_i32 s10, s10, 0xc8000
	s_add_i32 s11, s11, s10
	s_mul_i32 s8, s8, 0xc8000
	s_and_b32 s22, s2, 7
	s_waitcnt lgkmcnt(0)
	s_add_u32 s4, s4, s8
	s_mul_i32 s8, s22, 0x1900
	v_add_u32_e32 v137, s8, v0
	s_addc_u32 s5, s5, s11
	v_lshlrev_b32_e32 v74, 4, v137
	v_mov_b32_e32 v75, 0
	v_lshl_add_u64 v[130:131], s[4:5], 0, v[74:75]
	global_load_dwordx4 v[46:49], v74, s[4:5] sc0 nt
	s_mov_b32 s4, 0xc80000
	v_add_co_u32_e32 v2, vcc, s4, v130
	s_mov_b32 s4, 0x1900000
	s_nop 0
	v_addc_co_u32_e32 v3, vcc, 0, v131, vcc
	global_load_dwordx4 v[26:29], v[2:3], off sc0 nt
	v_add_co_u32_e32 v2, vcc, s4, v130
	s_mov_b32 s5, 0x3200000
	s_nop 0
	v_addc_co_u32_e32 v3, vcc, 0, v131, vcc
	global_load_dwordx4 v[34:37], v[2:3], off sc0 nt
	v_add_co_u32_e32 v2, vcc, s5, v130
	s_mov_b32 s4, 0x2580000
	s_nop 0
	v_addc_co_u32_e32 v3, vcc, 0, v131, vcc
	s_mul_hi_i32 s5, s9, 0xc8000
	s_mul_i32 s9, s9, 0xc8000
	global_load_dwordx4 v[18:21], v[2:3], off sc0 nt
	v_add_co_u32_e32 v2, vcc, s4, v130
	s_add_u32 s4, s6, s9
	s_nop 0
	v_addc_co_u32_e32 v3, vcc, 0, v131, vcc
	s_addc_u32 s5, s7, s5
	global_load_dwordx4 v[10:13], v[2:3], off sc0 nt
	global_load_dwordx4 v[6:9], v74, s[4:5] sc0 nt
	v_cvt_f32_ubyte0_e32 v1, s3
	v_mov_b32_e32 v2, 1.0
	s_movk_i32 s6, 0x3000
	v_fmamk_f32 v128, v1, 0x3b53680d, v2
	v_add_co_u32_e32 v2, vcc, s6, v130
	s_mov_b32 s7, 0xc83000
	s_nop 0
	v_addc_co_u32_e32 v3, vcc, 0, v131, vcc
	v_add_co_u32_e32 v4, vcc, s7, v130
	s_mov_b32 s7, 0x1903000
	s_nop 0
	v_addc_co_u32_e32 v5, vcc, 0, v131, vcc
	global_load_dwordx4 v[38:41], v[2:3], off sc0 nt
	global_load_dwordx4 v[30:33], v[4:5], off sc0 nt
	v_add_co_u32_e32 v2, vcc, s7, v130
	s_mov_b32 s7, 0x2583000
	s_nop 0
	v_addc_co_u32_e32 v3, vcc, 0, v131, vcc
	v_add_co_u32_e32 v4, vcc, s7, v130
	s_mov_b32 s7, 0x3203000
	s_nop 0
	v_addc_co_u32_e32 v5, vcc, 0, v131, vcc
	global_load_dwordx4 v[42:45], v[2:3], off sc0 nt
	global_load_dwordx4 v[14:17], v[4:5], off sc0 nt
	v_add_co_u32_e32 v2, vcc, s7, v130
	v_lshl_add_u64 v[132:133], s[4:5], 0, v[74:75]
	s_nop 0
	v_addc_co_u32_e32 v3, vcc, 0, v131, vcc
	global_load_dwordx4 v[22:25], v[2:3], off sc0 nt
	v_add_co_u32_e32 v2, vcc, s6, v132
	s_mov_b32 s6, 0xcccd
	s_nop 0
	v_addc_co_u32_e32 v3, vcc, 0, v133, vcc
	global_load_dwordx4 v[2:5], v[2:3], off sc0 nt
	v_mul_u32_u24_sdwa v1, v137, s6 dst_sel:DWORD dst_unused:UNUSED_PAD src0_sel:WORD_0 src1_sel:DWORD
	v_lshrrev_b32_e32 v1, 23, v1
	v_cvt_f32_u32_e32 v50, v1
	v_mul_i32_i24_e32 v1, 0xffffff60, v1
	v_add_lshl_u32 v1, v1, v137, 2
	v_cvt_f32_i32_e32 v1, v1
	s_mov_b32 s7, 0x3b033c6e
	v_fma_f32 v50, v50, s7, 1.0
	s_mov_b32 s9, 0x3b086211
	v_fma_f32 v1, v1, s9, 1.0
	v_add_f32_e32 v59, 0x3b086211, v1
	v_mov_b32_e32 v136, 0x670
	s_waitcnt vmcnt(11)
	v_mul_f32_e32 v46, 0x4038aa3b, v46
	v_exp_f32_e32 v46, v46
	v_mul_f32_e32 v47, 0x4038aa3b, v47
	v_exp_f32_e32 v47, v47
	v_mul_f32_e32 v48, 0x4038aa3b, v48
	v_add_f32_e32 v46, 1.0, v46
	v_rcp_f32_e32 v46, v46
	s_waitcnt vmcnt(10)
	v_mul_f32_e32 v26, 0x4038aa3b, v26
	v_exp_f32_e32 v26, v26
	v_mul_f32_e32 v27, 0x4038aa3b, v27
	v_exp_f32_e32 v27, v27
	v_fma_f32 v46, -2.0, v46, v128
	v_add_f32_e32 v26, 1.0, v26
	s_waitcnt vmcnt(9)
	v_mul_f32_e32 v34, 0x4038aa3b, v34
	v_exp_f32_e32 v34, v34
	v_mul_f32_e32 v35, 0x4038aa3b, v35
	v_rcp_f32_e32 v26, v26
	v_exp_f32_e32 v35, v35
	v_add_f32_e32 v34, 1.0, v34
	v_rcp_f32_e32 v34, v34
	v_fma_f32 v26, -2.0, v26, v50
	v_add_f32_e32 v47, 1.0, v47
	v_add_f32_e32 v27, 1.0, v27
	v_add_f32_e32 v35, 1.0, v35
	v_fma_f32 v34, -2.0, v34, v1
	v_add_f32_e32 v51, v46, v26
	v_rcp_f32_e32 v47, v47
	v_rcp_f32_e32 v27, v27
	v_rcp_f32_e32 v35, v35
	v_add_f32_e32 v76, v51, v34
	v_mul_f32_e32 v78, v34, v34
	v_fmac_f32_e32 v78, v26, v26
	s_waitcnt vmcnt(7)
	v_mul_f32_e32 v26, v10, v10
	s_waitcnt vmcnt(6)
	v_cmp_eq_u32_e32 vcc, 1, v6
	v_add_f32_e32 v51, 0, v76
	v_add_f32_e32 v10, 0, v10
	v_fmac_f32_e32 v78, v46, v46
	v_cndmask_b32_e64 v34, 0, 1.0, vcc
	v_cndmask_b32_e32 v46, 0, v26, vcc
	v_cndmask_b32_e32 v52, 0, v51, vcc
	v_cndmask_b32_e32 v53, 0, v10, vcc
	v_cmp_eq_u32_e32 vcc, 2, v6
	v_fma_f32 v47, -2.0, v47, v128
	v_fma_f32 v27, -2.0, v27, v50
	v_cndmask_b32_e64 v54, 0, 1.0, vcc
	v_cndmask_b32_e32 v55, 0, v26, vcc
	v_cndmask_b32_e32 v56, 0, v51, vcc
	v_cndmask_b32_e32 v57, 0, v10, vcc
	v_cmp_eq_u32_e32 vcc, 3, v6
	v_fmac_f32_e32 v59, -2.0, v35
	v_add_f32_e32 v35, v47, v27
	v_cndmask_b32_e64 v58, 0, 1.0, vcc
	v_cndmask_b32_e32 v26, 0, v26, vcc
	v_cndmask_b32_e32 v51, 0, v51, vcc
	v_cndmask_b32_e32 v10, 0, v10, vcc
	v_mul_f32_e32 v79, v59, v59
	v_cmp_eq_u32_e32 vcc, 1, v7
	v_add_f32_e32 v77, v35, v59
	v_fmac_f32_e32 v79, v27, v27
	v_mul_f32_e32 v27, v11, v11
	v_cndmask_b32_e64 v35, 0, 1.0, vcc
	v_fmac_f32_e32 v79, v47, v47
	v_add_f32_e32 v34, v35, v34
	v_cndmask_b32_e32 v35, 0, v27, vcc
	v_cndmask_b32_e32 v47, 0, v11, vcc
	v_cndmask_b32_e32 v59, 0, v77, vcc
	v_cmp_eq_u32_e32 vcc, 2, v7
	v_add_f32_e32 v35, v35, v46
	v_add_f32_e32 v52, v52, v59
	v_cndmask_b32_e64 v46, 0, 1.0, vcc
	v_add_f32_e32 v47, v47, v53
	v_add_f32_e32 v46, v46, v54
	v_cndmask_b32_e32 v53, 0, v27, vcc
	v_cndmask_b32_e32 v54, 0, v11, vcc
	v_cndmask_b32_e32 v59, 0, v77, vcc
	v_cmp_eq_u32_e32 vcc, 3, v7
	v_exp_f32_e32 v48, v48
	v_add_f32_e32 v54, v54, v57
	v_cndmask_b32_e32 v27, 0, v27, vcc
	v_cndmask_b32_e32 v11, 0, v11, vcc
	v_add_f32_e32 v10, v11, v10
	v_add_f32_e32 v11, v27, v26
	v_mul_f32_e32 v27, 0x4038aa3b, v28
	v_mul_f32_e32 v28, 0x4038aa3b, v36
	v_exp_f32_e32 v28, v28
	v_exp_f32_e32 v27, v27
	v_add_f32_e32 v26, 1.0, v48
	v_rcp_f32_e32 v26, v26
	v_add_f32_e32 v28, 1.0, v28
	v_add_f32_e32 v27, 1.0, v27
	v_rcp_f32_e32 v28, v28
	v_rcp_f32_e32 v27, v27
	v_add_f32_e32 v36, 0x3b886211, v1
	v_fma_f32 v26, -2.0, v26, v128
	v_fmac_f32_e32 v36, -2.0, v28
	v_fma_f32 v27, -2.0, v27, v50
	v_mul_f32_e32 v82, v36, v36
	v_add_f32_e32 v53, v53, v55
	v_cndmask_b32_e64 v55, 0, 1.0, vcc
	v_cndmask_b32_e32 v57, 0, v77, vcc
	v_add_f32_e32 v28, v26, v27
	v_fmac_f32_e32 v82, v27, v27
	v_cmp_eq_u32_e32 vcc, 1, v8
	v_add_f32_e32 v80, v28, v36
	v_fmac_f32_e32 v82, v26, v26
	v_mul_f32_e32 v26, v12, v12
	v_cndmask_b32_e64 v27, 0, 1.0, vcc
	v_add_f32_e32 v27, v27, v34
	v_cndmask_b32_e32 v28, 0, v26, vcc
	v_cndmask_b32_e32 v34, 0, v12, vcc
	v_cndmask_b32_e32 v36, 0, v80, vcc
	v_cmp_eq_u32_e32 vcc, 2, v8
	v_add_f32_e32 v28, v28, v35
	v_add_f32_e32 v34, v34, v47
	v_cndmask_b32_e64 v35, 0, 1.0, vcc
	v_add_f32_e32 v35, v35, v46
	v_cndmask_b32_e32 v46, 0, v26, vcc
	v_cndmask_b32_e32 v47, 0, v12, vcc
	v_cndmask_b32_e32 v48, 0, v80, vcc
	v_cmp_eq_u32_e32 vcc, 3, v8
	v_mul_f32_e32 v49, 0x4038aa3b, v49
	v_exp_f32_e32 v49, v49
	v_cndmask_b32_e32 v26, 0, v26, vcc
	v_add_f32_e32 v11, v26, v11
	v_mul_f32_e32 v26, 0x4038aa3b, v29
	v_mul_f32_e32 v29, 0x4038aa3b, v37
	v_exp_f32_e32 v26, v26
	v_exp_f32_e32 v29, v29
	v_cndmask_b32_e32 v12, 0, v12, vcc
	v_add_f32_e32 v10, v12, v10
	v_add_f32_e32 v12, 1.0, v49
	v_add_f32_e32 v26, 1.0, v26
	v_add_f32_e32 v29, 1.0, v29
	v_rcp_f32_e32 v12, v12
	v_rcp_f32_e32 v26, v26
	v_rcp_f32_e32 v29, v29
	v_mul_f32_e32 v21, 0xbfb8aa3b, v21
	v_exp_f32_e32 v21, v21
	v_add_f32_e32 v1, 0x3bcc931a, v1
	v_mul_f32_e32 v18, 0xbfb8aa3b, v18
	v_mul_f32_e32 v19, 0xbfb8aa3b, v19
	v_mul_f32_e32 v20, 0xbfb8aa3b, v20
	v_fma_f32 v12, -2.0, v12, v128
	v_fmac_f32_e32 v50, -2.0, v26
	v_fmac_f32_e32 v1, -2.0, v29
	v_exp_f32_e32 v18, v18
	v_exp_f32_e32 v19, v19
	v_exp_f32_e32 v20, v20
	v_add_f32_e32 v26, v12, v50
	v_mul_f32_e32 v83, v1, v1
	v_add_f32_e32 v36, v52, v36
	v_add_f32_e32 v46, v46, v53
	v_cndmask_b32_e64 v52, 0, 1.0, vcc
	v_cndmask_b32_e32 v53, 0, v80, vcc
	v_add_f32_e32 v81, v26, v1
	v_fmac_f32_e32 v83, v50, v50
	v_add_f32_e32 v1, 1.0, v21
	v_cmp_eq_u32_e32 vcc, 1, v9
	v_fmac_f32_e32 v83, v12, v12
	v_rcp_f32_e32 v21, v1
	v_mul_f32_e32 v1, v13, v13
	v_cndmask_b32_e64 v12, 0, 1.0, vcc
	v_add_f32_e32 v47, v47, v54
	v_add_f32_e32 v54, v12, v27
	v_cndmask_b32_e32 v12, 0, v1, vcc
	v_cndmask_b32_e32 v26, 0, v13, vcc
	v_cndmask_b32_e32 v27, 0, v81, vcc
	v_cmp_eq_u32_e32 vcc, 2, v9
	v_add_f32_e32 v18, 1.0, v18
	v_add_f32_e32 v19, 1.0, v19
	v_add_f32_e32 v56, v56, v59
	v_add_f32_e32 v55, v55, v58
	v_add_f32_e32 v51, v51, v57
	v_add_f32_e32 v20, 1.0, v20
	v_add_f32_e32 v57, v12, v28
	v_cndmask_b32_e64 v12, 0, 1.0, vcc
	v_rcp_f32_e32 v18, v18
	v_rcp_f32_e32 v19, v19
	v_rcp_f32_e32 v20, v20
	v_add_f32_e32 v48, v56, v48
	v_add_f32_e32 v52, v52, v55
	v_add_f32_e32 v55, v36, v27
	v_add_f32_e32 v56, v26, v34
	v_add_f32_e32 v58, v12, v35
	v_cndmask_b32_e32 v12, 0, v1, vcc
	v_cndmask_b32_e32 v26, 0, v13, vcc
	v_cndmask_b32_e32 v27, 0, v81, vcc
	v_cmp_eq_u32_e32 vcc, 3, v9
	v_add_f32_e32 v61, v12, v46
	s_movk_i32 s4, 0x100
	v_cndmask_b32_e64 v12, 0, 1.0, vcc
	v_add_f32_e32 v51, v51, v53
	v_add_f32_e32 v62, v12, v52
	v_cndmask_b32_e32 v1, 0, v1, vcc
	v_cndmask_b32_e32 v12, 0, v13, vcc
	v_cndmask_b32_e32 v13, 0, v81, vcc
	v_lshl_add_u32 v134, v0, 4, v136
	v_cmp_gt_u32_e64 s[4:5], s4, v0
	v_add_f32_e32 v59, v48, v27
	v_add_f32_e32 v60, v26, v47
	v_add_f32_e32 v63, v51, v13
	v_add_f32_e32 v64, v12, v10
	v_add_f32_e32 v65, v1, v11
	s_mov_b32 s10, 0xc000
	v_add_u32_e32 v1, 0xc000, v134
	ds_write_b128 v134, v[18:21] offset:49152
	s_movk_i32 s11, 0x6000
	v_add_co_u32_e32 v10, vcc, s11, v130
	s_mov_b32 s12, 0xc86000
	s_nop 0
	v_addc_co_u32_e32 v11, vcc, 0, v131, vcc
	v_add_co_u32_e32 v12, vcc, s12, v130
	s_mov_b32 s12, 0x1906000
	s_nop 0
	v_addc_co_u32_e32 v13, vcc, 0, v131, vcc
	global_load_dwordx4 v[46:49], v[10:11], off sc0 nt
	global_load_dwordx4 v[34:37], v[12:13], off sc0 nt
	v_add_co_u32_e32 v10, vcc, s12, v130
	s_mov_b32 s12, 0x2586000
	s_nop 0
	v_addc_co_u32_e32 v11, vcc, 0, v131, vcc
	v_add_co_u32_e32 v12, vcc, s12, v130
	s_mov_b32 s12, 0x3206000
	s_nop 0
	v_addc_co_u32_e32 v13, vcc, 0, v131, vcc
	global_load_dwordx4 v[50:53], v[10:11], off sc0 nt
	global_load_dwordx4 v[18:21], v[12:13], off sc0 nt
	v_add_co_u32_e32 v10, vcc, s12, v130
	v_add_u32_e32 v66, 0x300, v137
	s_nop 0
	v_addc_co_u32_e32 v11, vcc, 0, v131, vcc
	global_load_dwordx4 v[26:29], v[10:11], off sc0 nt
	v_add_co_u32_e32 v10, vcc, s11, v132
	s_waitcnt vmcnt(8)
	v_mul_f32_e32 v42, 0x4038aa3b, v42
	v_addc_co_u32_e32 v11, vcc, 0, v133, vcc
	global_load_dwordx4 v[10:13], v[10:11], off sc0 nt
	v_mul_u32_u24_sdwa v67, v66, s6 dst_sel:DWORD dst_unused:UNUSED_PAD src0_sel:WORD_0 src1_sel:DWORD
	v_mul_f32_e32 v38, 0x4038aa3b, v38
	v_mul_f32_e32 v30, 0x4038aa3b, v30
	v_exp_f32_e32 v42, v42
	v_lshrrev_b32_e32 v67, 23, v67
	v_exp_f32_e32 v38, v38
	v_exp_f32_e32 v30, v30
	v_cvt_f32_u32_e32 v68, v67
	v_mul_i32_i24_e32 v67, 0xffffff60, v67
	v_add_lshl_u32 v66, v67, v66, 2
	v_cvt_f32_i32_e32 v66, v66
	v_add_f32_e32 v42, 1.0, v42
	v_add_f32_e32 v38, 1.0, v38
	v_add_f32_e32 v30, 1.0, v30
	v_rcp_f32_e32 v42, v42
	v_rcp_f32_e32 v38, v38
	v_rcp_f32_e32 v30, v30
	v_fma_f32 v66, v66, s9, 1.0
	v_mul_f32_e32 v43, 0x4038aa3b, v43
	v_fma_f32 v68, v68, s7, 1.0
	v_fma_f32 v42, -2.0, v42, v66
	v_mul_f32_e32 v39, 0x4038aa3b, v39
	v_mul_f32_e32 v31, 0x4038aa3b, v31
	v_exp_f32_e32 v43, v43
	v_fma_f32 v38, -2.0, v38, v128
	v_fma_f32 v30, -2.0, v30, v68
	v_mul_f32_e32 v86, v42, v42
	v_exp_f32_e32 v39, v39
	v_exp_f32_e32 v31, v31
	v_add_f32_e32 v67, v38, v30
	v_fmac_f32_e32 v86, v30, v30
	s_waitcnt vmcnt(6)
	v_cmp_eq_u32_e32 vcc, 1, v2
	v_add_f32_e32 v84, v67, v42
	v_fmac_f32_e32 v86, v38, v38
	v_mul_f32_e32 v30, v14, v14
	v_cndmask_b32_e64 v38, 0, 1.0, vcc
	v_add_f32_e32 v38, v54, v38
	v_cndmask_b32_e32 v42, 0, v30, vcc
	v_cndmask_b32_e32 v54, 0, v14, vcc
	v_cndmask_b32_e32 v67, 0, v84, vcc
	v_cmp_eq_u32_e32 vcc, 2, v2
	v_add_f32_e32 v43, 1.0, v43
	v_add_f32_e32 v54, v56, v54
	v_cndmask_b32_e64 v56, 0, 1.0, vcc
	v_add_f32_e32 v39, 1.0, v39
	v_add_f32_e32 v31, 1.0, v31
	v_rcp_f32_e32 v43, v43
	v_add_f32_e32 v55, v55, v67
	v_add_f32_e32 v42, v57, v42
	v_add_f32_e32 v56, v58, v56
	v_cndmask_b32_e32 v57, 0, v30, vcc
	v_cndmask_b32_e32 v58, 0, v14, vcc
	v_cndmask_b32_e32 v67, 0, v84, vcc
	v_cmp_eq_u32_e32 vcc, 3, v2
	v_rcp_f32_e32 v39, v39
	v_rcp_f32_e32 v31, v31
	v_add_f32_e32 v58, v60, v58
	v_cndmask_b32_e64 v60, 0, 1.0, vcc
	v_add_f32_e32 v60, v62, v60
	v_add_f32_e32 v62, 0x3b086211, v66
	v_fmac_f32_e32 v62, -2.0, v43
	v_fma_f32 v39, -2.0, v39, v128
	v_fma_f32 v31, -2.0, v31, v68
	v_mul_f32_e32 v87, v62, v62
	v_add_f32_e32 v57, v61, v57
	v_cndmask_b32_e32 v30, 0, v30, vcc
	v_cndmask_b32_e32 v14, 0, v14, vcc
	v_cndmask_b32_e32 v61, 0, v84, vcc
	v_add_f32_e32 v43, v39, v31
	v_fmac_f32_e32 v87, v31, v31
	v_cmp_eq_u32_e32 vcc, 1, v3
	v_add_f32_e32 v85, v43, v62
	v_fmac_f32_e32 v87, v39, v39
	v_mul_f32_e32 v31, v15, v15
	v_cndmask_b32_e64 v39, 0, 1.0, vcc
	v_add_f32_e32 v38, v39, v38
	v_cndmask_b32_e32 v39, 0, v31, vcc
	v_cndmask_b32_e32 v43, 0, v15, vcc
	v_cndmask_b32_e32 v62, 0, v85, vcc
	v_cmp_eq_u32_e32 vcc, 2, v3
	v_add_f32_e32 v39, v39, v42
	v_add_f32_e32 v55, v55, v62
	v_cndmask_b32_e64 v42, 0, 1.0, vcc
	v_add_f32_e32 v43, v43, v54
	v_add_f32_e32 v42, v42, v56
	v_cndmask_b32_e32 v54, 0, v31, vcc
	v_cndmask_b32_e32 v56, 0, v15, vcc
	v_cndmask_b32_e32 v62, 0, v85, vcc
	v_cmp_eq_u32_e32 vcc, 3, v3
	v_add_f32_e32 v14, v64, v14
	v_add_f32_e32 v30, v65, v30
	v_cndmask_b32_e32 v31, 0, v31, vcc
	v_cndmask_b32_e32 v15, 0, v15, vcc
	v_add_f32_e32 v14, v15, v14
	v_add_f32_e32 v15, v31, v30
	v_mul_f32_e32 v31, 0x4038aa3b, v32
	v_mul_f32_e32 v32, 0x4038aa3b, v44
	v_mul_f32_e32 v40, 0x4038aa3b, v40
	v_exp_f32_e32 v32, v32
	v_exp_f32_e32 v40, v40
	v_exp_f32_e32 v31, v31
	v_add_f32_e32 v56, v56, v58
	v_add_f32_e32 v32, 1.0, v32
	v_add_f32_e32 v30, 1.0, v40
	v_add_f32_e32 v31, 1.0, v31
	v_rcp_f32_e32 v32, v32
	v_rcp_f32_e32 v30, v30
	v_rcp_f32_e32 v31, v31
	v_add_f32_e32 v40, 0x3b886211, v66
	v_fmac_f32_e32 v40, -2.0, v32
	v_fma_f32 v30, -2.0, v30, v128
	v_fma_f32 v31, -2.0, v31, v68
	v_mul_f32_e32 v90, v40, v40
	v_add_f32_e32 v54, v54, v57
	v_cndmask_b32_e64 v57, 0, 1.0, vcc
	v_cndmask_b32_e32 v58, 0, v85, vcc
	v_add_f32_e32 v32, v30, v31
	v_fmac_f32_e32 v90, v31, v31
	v_cmp_eq_u32_e32 vcc, 1, v4
	v_add_f32_e32 v88, v32, v40
	v_fmac_f32_e32 v90, v30, v30
	v_mul_f32_e32 v30, v16, v16
	v_cndmask_b32_e64 v31, 0, 1.0, vcc
	v_add_f32_e32 v31, v31, v38
	v_cndmask_b32_e32 v32, 0, v30, vcc
	v_cndmask_b32_e32 v38, 0, v16, vcc
	v_cndmask_b32_e32 v40, 0, v88, vcc
	v_cmp_eq_u32_e32 vcc, 2, v4
	v_add_f32_e32 v32, v32, v39
	v_add_f32_e32 v38, v38, v43
	v_cndmask_b32_e64 v39, 0, 1.0, vcc
	v_add_f32_e32 v39, v39, v42
	v_cndmask_b32_e32 v42, 0, v30, vcc
	v_cndmask_b32_e32 v43, 0, v16, vcc
	v_cndmask_b32_e32 v44, 0, v88, vcc
	v_cmp_eq_u32_e32 vcc, 3, v4
	v_mul_f32_e32 v41, 0x4038aa3b, v41
	v_exp_f32_e32 v41, v41
	v_cndmask_b32_e32 v30, 0, v30, vcc
	v_add_f32_e32 v15, v30, v15
	v_mul_f32_e32 v30, 0x4038aa3b, v33
	v_mul_f32_e32 v33, 0x4038aa3b, v45
	v_exp_f32_e32 v33, v33
	v_exp_f32_e32 v30, v30
	v_cndmask_b32_e32 v16, 0, v16, vcc
	v_add_f32_e32 v14, v16, v14
	v_add_f32_e32 v33, 1.0, v33
	v_add_f32_e32 v30, 1.0, v30
	v_rcp_f32_e32 v33, v33
	v_add_f32_e32 v16, 1.0, v41
	v_rcp_f32_e32 v30, v30
	v_rcp_f32_e32 v16, v16
	v_mul_f32_e32 v25, 0xbfb8aa3b, v25
	v_add_f32_e32 v41, 0x3bcc931a, v66
	v_exp_f32_e32 v25, v25
	v_fmac_f32_e32 v41, -2.0, v33
	v_mul_f32_e32 v22, 0xbfb8aa3b, v22
	v_mul_f32_e32 v23, 0xbfb8aa3b, v23
	v_mul_f32_e32 v24, 0xbfb8aa3b, v24
	v_fmac_f32_e32 v68, -2.0, v30
	v_mul_f32_e32 v91, v41, v41
	v_exp_f32_e32 v22, v22
	v_exp_f32_e32 v23, v23
	v_exp_f32_e32 v24, v24
	v_fma_f32 v16, -2.0, v16, v128
	v_fmac_f32_e32 v91, v68, v68
	v_add_f32_e32 v40, v55, v40
	v_add_f32_e32 v42, v42, v54
	v_cndmask_b32_e64 v54, 0, 1.0, vcc
	v_cndmask_b32_e32 v55, 0, v88, vcc
	v_add_f32_e32 v30, v16, v68
	v_fmac_f32_e32 v91, v16, v16
	v_add_f32_e32 v16, 1.0, v25
	v_cmp_eq_u32_e32 vcc, 1, v5
	v_add_f32_e32 v89, v30, v41
	v_rcp_f32_e32 v25, v16
	v_mul_f32_e32 v16, v17, v17
	v_cndmask_b32_e64 v30, 0, 1.0, vcc
	v_add_f32_e32 v45, v30, v31
	v_cndmask_b32_e32 v30, 0, v16, vcc
	v_cndmask_b32_e32 v31, 0, v17, vcc
	v_cndmask_b32_e32 v33, 0, v89, vcc
	v_cmp_eq_u32_e32 vcc, 2, v5
	v_add_f32_e32 v22, 1.0, v22
	v_add_f32_e32 v23, 1.0, v23
	v_add_f32_e32 v57, v57, v60
	v_add_f32_e32 v24, 1.0, v24
	v_add_f32_e32 v66, v30, v32
	v_cndmask_b32_e64 v30, 0, 1.0, vcc
	v_rcp_f32_e32 v22, v22
	v_add_f32_e32 v59, v59, v67
	v_add_f32_e32 v61, v63, v61
	v_rcp_f32_e32 v23, v23
	v_rcp_f32_e32 v24, v24
	v_add_f32_e32 v54, v54, v57
	v_add_f32_e32 v57, v31, v38
	v_add_f32_e32 v67, v30, v39
	v_cndmask_b32_e32 v30, 0, v16, vcc
	v_cndmask_b32_e32 v31, 0, v17, vcc
	v_cndmask_b32_e32 v32, 0, v89, vcc
	v_cmp_eq_u32_e32 vcc, 3, v5
	v_add_f32_e32 v58, v61, v58
	v_add_f32_e32 v42, v30, v42
	v_cndmask_b32_e64 v30, 0, 1.0, vcc
	v_add_f32_e32 v59, v59, v62
	v_add_f32_e32 v55, v58, v55
	v_add_f32_e32 v54, v30, v54
	v_cndmask_b32_e32 v16, 0, v16, vcc
	v_cndmask_b32_e32 v17, 0, v17, vcc
	v_cndmask_b32_e32 v30, 0, v89, vcc
	v_add_f32_e32 v44, v59, v44
	v_add_f32_e32 v43, v43, v56
	v_add_f32_e32 v55, v55, v30
	v_add_f32_e32 v68, v17, v14
	v_add_f32_e32 v69, v16, v15
	v_add_f32_e32 v56, v40, v33
	v_add_f32_e32 v44, v44, v32
	v_add_f32_e32 v43, v31, v43
	ds_write_b128 v134, v[22:25] offset:61440
	s_mov_b32 s11, 0x9000
	v_add_co_u32_e32 v14, vcc, s11, v130
	s_mov_b32 s12, 0xc89000
	s_nop 0
	v_addc_co_u32_e32 v15, vcc, 0, v131, vcc
	v_add_co_u32_e32 v16, vcc, s12, v130
	s_mov_b32 s12, 0x1909000
	s_nop 0
	v_addc_co_u32_e32 v17, vcc, 0, v131, vcc
	global_load_dwordx4 v[62:65], v[14:15], off sc0 nt
	global_load_dwordx4 v[38:41], v[16:17], off sc0 nt
	v_add_co_u32_e32 v14, vcc, s12, v130
	s_mov_b32 s12, 0x2589000
	s_nop 0
	v_addc_co_u32_e32 v15, vcc, 0, v131, vcc
	v_add_co_u32_e32 v16, vcc, s12, v130
	s_mov_b32 s12, 0x3209000
	s_nop 0
	v_addc_co_u32_e32 v17, vcc, 0, v131, vcc
	global_load_dwordx4 v[58:61], v[14:15], off sc0 nt
	global_load_dwordx4 v[22:25], v[16:17], off sc0 nt
	v_add_co_u32_e32 v14, vcc, s12, v130
	v_add_u32_e32 v70, 0x600, v137
	s_nop 0
	v_addc_co_u32_e32 v15, vcc, 0, v131, vcc
	global_load_dwordx4 v[30:33], v[14:15], off sc0 nt
	v_add_co_u32_e32 v14, vcc, s11, v132
	s_waitcnt vmcnt(8)
	v_mul_f32_e32 v50, 0x4038aa3b, v50
	v_addc_co_u32_e32 v15, vcc, 0, v133, vcc
	global_load_dwordx4 v[14:17], v[14:15], off sc0 nt
	v_mul_u32_u24_sdwa v71, v70, s6 dst_sel:DWORD dst_unused:UNUSED_PAD src0_sel:WORD_0 src1_sel:DWORD
	v_mul_f32_e32 v46, 0x4038aa3b, v46
	v_mul_f32_e32 v34, 0x4038aa3b, v34
	v_exp_f32_e32 v50, v50
	v_lshrrev_b32_e32 v71, 23, v71
	v_exp_f32_e32 v46, v46
	v_exp_f32_e32 v34, v34
	v_cvt_f32_u32_e32 v72, v71
	v_mul_i32_i24_e32 v71, 0xffffff60, v71
	v_add_lshl_u32 v70, v71, v70, 2
	v_cvt_f32_i32_e32 v70, v70
	v_add_f32_e32 v50, 1.0, v50
	v_add_f32_e32 v46, 1.0, v46
	v_add_f32_e32 v34, 1.0, v34
	v_rcp_f32_e32 v50, v50
	v_rcp_f32_e32 v46, v46
	v_rcp_f32_e32 v34, v34
	v_fma_f32 v70, v70, s9, 1.0
	v_fma_f32 v72, v72, s7, 1.0
	v_fma_f32 v50, -2.0, v50, v70
	v_mul_f32_e32 v51, 0x4038aa3b, v51
	v_fma_f32 v46, -2.0, v46, v128
	v_fma_f32 v34, -2.0, v34, v72
	v_mul_f32_e32 v94, v50, v50
	v_mul_f32_e32 v47, 0x4038aa3b, v47
	v_mul_f32_e32 v35, 0x4038aa3b, v35
	v_exp_f32_e32 v51, v51
	v_add_f32_e32 v71, v46, v34
	v_fmac_f32_e32 v94, v34, v34
	s_waitcnt vmcnt(6)
	v_cmp_eq_u32_e32 vcc, 1, v10
	v_exp_f32_e32 v47, v47
	v_exp_f32_e32 v35, v35
	v_add_f32_e32 v92, v71, v50
	v_fmac_f32_e32 v94, v46, v46
	v_mul_f32_e32 v34, v18, v18
	v_cndmask_b32_e64 v46, 0, 1.0, vcc
	v_add_f32_e32 v45, v45, v46
	v_cndmask_b32_e32 v46, 0, v34, vcc
	v_cndmask_b32_e32 v50, 0, v18, vcc
	v_cndmask_b32_e32 v71, 0, v92, vcc
	v_cmp_eq_u32_e32 vcc, 2, v10
	v_add_f32_e32 v50, v57, v50
	v_add_f32_e32 v51, 1.0, v51
	v_cndmask_b32_e64 v57, 0, 1.0, vcc
	v_add_f32_e32 v56, v56, v71
	v_add_f32_e32 v46, v66, v46
	v_add_f32_e32 v57, v67, v57
	v_cndmask_b32_e32 v66, 0, v34, vcc
	v_cndmask_b32_e32 v67, 0, v18, vcc
	v_cndmask_b32_e32 v71, 0, v92, vcc
	v_cmp_eq_u32_e32 vcc, 3, v10
	v_add_f32_e32 v47, 1.0, v47
	v_add_f32_e32 v35, 1.0, v35
	v_rcp_f32_e32 v51, v51
	v_add_f32_e32 v42, v42, v66
	v_cndmask_b32_e64 v66, 0, 1.0, vcc
	v_rcp_f32_e32 v47, v47
	v_rcp_f32_e32 v35, v35
	v_add_f32_e32 v54, v54, v66
	v_cndmask_b32_e32 v66, 0, v92, vcc
	v_add_f32_e32 v55, v55, v66
	v_add_f32_e32 v66, 0x3b086211, v70
	v_fmac_f32_e32 v66, -2.0, v51
	v_fma_f32 v47, -2.0, v47, v128
	v_fma_f32 v35, -2.0, v35, v72
	v_mul_f32_e32 v95, v66, v66
	v_cndmask_b32_e32 v34, 0, v34, vcc
	v_cndmask_b32_e32 v18, 0, v18, vcc
	v_add_f32_e32 v51, v47, v35
	v_fmac_f32_e32 v95, v35, v35
	v_cmp_eq_u32_e32 vcc, 1, v11
	v_add_f32_e32 v93, v51, v66
	v_fmac_f32_e32 v95, v47, v47
	v_mul_f32_e32 v35, v19, v19
	v_cndmask_b32_e64 v47, 0, 1.0, vcc
	v_add_f32_e32 v45, v47, v45
	v_cndmask_b32_e32 v47, 0, v35, vcc
	v_cndmask_b32_e32 v51, 0, v19, vcc
	v_cndmask_b32_e32 v66, 0, v93, vcc
	v_cmp_eq_u32_e32 vcc, 2, v11
	v_add_f32_e32 v46, v47, v46
	v_add_f32_e32 v56, v56, v66
	v_cndmask_b32_e64 v47, 0, 1.0, vcc
	v_add_f32_e32 v50, v51, v50
	v_add_f32_e32 v47, v47, v57
	v_cndmask_b32_e32 v51, 0, v35, vcc
	v_cndmask_b32_e32 v57, 0, v19, vcc
	v_cndmask_b32_e32 v66, 0, v93, vcc
	v_cmp_eq_u32_e32 vcc, 3, v11
	v_add_f32_e32 v18, v68, v18
	v_add_f32_e32 v34, v69, v34
	v_cndmask_b32_e32 v35, 0, v35, vcc
	v_cndmask_b32_e32 v19, 0, v19, vcc
	v_add_f32_e32 v18, v19, v18
	v_add_f32_e32 v19, v35, v34
	v_mul_f32_e32 v35, 0x4038aa3b, v36
	v_mul_f32_e32 v36, 0x4038aa3b, v52
	v_mul_f32_e32 v48, 0x4038aa3b, v48
	v_exp_f32_e32 v36, v36
	v_exp_f32_e32 v48, v48
	v_exp_f32_e32 v35, v35
	v_add_f32_e32 v42, v51, v42
	v_add_f32_e32 v36, 1.0, v36
	v_add_f32_e32 v34, 1.0, v48
	v_add_f32_e32 v35, 1.0, v35
	v_rcp_f32_e32 v36, v36
	v_rcp_f32_e32 v34, v34
	v_rcp_f32_e32 v35, v35
	v_add_f32_e32 v48, 0x3b886211, v70
	v_fmac_f32_e32 v48, -2.0, v36
	v_cndmask_b32_e64 v51, 0, 1.0, vcc
	v_fma_f32 v34, -2.0, v34, v128
	v_fma_f32 v35, -2.0, v35, v72
	v_mul_f32_e32 v98, v48, v48
	v_add_f32_e32 v51, v51, v54
	v_cndmask_b32_e32 v54, 0, v93, vcc
	v_add_f32_e32 v36, v34, v35
	v_fmac_f32_e32 v98, v35, v35
	v_cmp_eq_u32_e32 vcc, 1, v12
	v_add_f32_e32 v96, v36, v48
	v_fmac_f32_e32 v98, v34, v34
	v_mul_f32_e32 v34, v20, v20
	v_cndmask_b32_e64 v35, 0, 1.0, vcc
	v_add_f32_e32 v35, v35, v45
	v_cndmask_b32_e32 v36, 0, v34, vcc
	v_cndmask_b32_e32 v45, 0, v20, vcc
	v_cndmask_b32_e32 v48, 0, v96, vcc
	v_cmp_eq_u32_e32 vcc, 2, v12
	v_add_f32_e32 v36, v36, v46
	v_add_f32_e32 v45, v45, v50
	v_cndmask_b32_e64 v46, 0, 1.0, vcc
	v_add_f32_e32 v46, v46, v47
	v_cndmask_b32_e32 v47, 0, v34, vcc
	v_cndmask_b32_e32 v50, 0, v20, vcc
	v_cndmask_b32_e32 v52, 0, v96, vcc
	v_cmp_eq_u32_e32 vcc, 3, v12
	v_mul_f32_e32 v49, 0x4038aa3b, v49
	v_exp_f32_e32 v49, v49
	v_cndmask_b32_e32 v34, 0, v34, vcc
	v_add_f32_e32 v19, v34, v19
	v_mul_f32_e32 v34, 0x4038aa3b, v37
	v_mul_f32_e32 v37, 0x4038aa3b, v53
	v_exp_f32_e32 v37, v37
	v_exp_f32_e32 v34, v34
	v_cndmask_b32_e32 v20, 0, v20, vcc
	v_add_f32_e32 v18, v20, v18
	v_add_f32_e32 v37, 1.0, v37
	v_add_f32_e32 v34, 1.0, v34
	v_rcp_f32_e32 v37, v37
	v_add_f32_e32 v20, 1.0, v49
	v_rcp_f32_e32 v34, v34
	v_rcp_f32_e32 v20, v20
	v_mul_f32_e32 v29, 0xbfb8aa3b, v29
	v_add_f32_e32 v49, 0x3bcc931a, v70
	v_exp_f32_e32 v29, v29
	v_fmac_f32_e32 v49, -2.0, v37
	v_mul_f32_e32 v26, 0xbfb8aa3b, v26
	v_add_f32_e32 v43, v43, v67
	v_mul_f32_e32 v27, 0xbfb8aa3b, v27
	v_mul_f32_e32 v28, 0xbfb8aa3b, v28
	v_fmac_f32_e32 v72, -2.0, v34
	v_mul_f32_e32 v99, v49, v49
	v_exp_f32_e32 v26, v26
	v_exp_f32_e32 v27, v27
	v_add_f32_e32 v43, v57, v43
	v_exp_f32_e32 v28, v28
	v_fma_f32 v20, -2.0, v20, v128
	v_fmac_f32_e32 v99, v72, v72
	v_add_f32_e32 v43, v50, v43
	v_add_f32_e32 v42, v47, v42
	v_cndmask_b32_e64 v47, 0, 1.0, vcc
	v_cndmask_b32_e32 v50, 0, v96, vcc
	v_add_f32_e32 v34, v20, v72
	v_fmac_f32_e32 v99, v20, v20
	v_add_f32_e32 v20, 1.0, v29
	v_cmp_eq_u32_e32 vcc, 1, v13
	v_add_f32_e32 v97, v34, v49
	v_rcp_f32_e32 v29, v20
	v_mul_f32_e32 v20, v21, v21
	v_cndmask_b32_e64 v34, 0, 1.0, vcc
	v_add_f32_e32 v44, v44, v71
	v_add_f32_e32 v47, v47, v51
	v_add_f32_e32 v51, v34, v35
	v_cndmask_b32_e32 v34, 0, v20, vcc
	v_cndmask_b32_e32 v35, 0, v21, vcc
	v_cndmask_b32_e32 v37, 0, v97, vcc
	v_cmp_eq_u32_e32 vcc, 2, v13
	v_add_f32_e32 v26, 1.0, v26
	v_add_f32_e32 v27, 1.0, v27
	v_add_f32_e32 v44, v44, v66
	v_add_f32_e32 v28, 1.0, v28
	v_add_f32_e32 v66, v34, v36
	v_cndmask_b32_e64 v34, 0, 1.0, vcc
	v_rcp_f32_e32 v26, v26
	v_rcp_f32_e32 v27, v27
	v_rcp_f32_e32 v28, v28
	v_add_f32_e32 v53, v35, v45
	v_add_f32_e32 v67, v34, v46
	v_cndmask_b32_e32 v34, 0, v20, vcc
	v_cndmask_b32_e32 v35, 0, v21, vcc
	v_cndmask_b32_e32 v36, 0, v97, vcc
	v_cmp_eq_u32_e32 vcc, 3, v13
	v_add_f32_e32 v54, v55, v54
	v_add_f32_e32 v70, v34, v42
	v_cndmask_b32_e64 v34, 0, 1.0, vcc
	v_add_f32_e32 v44, v44, v52
	v_add_f32_e32 v50, v54, v50
	v_add_f32_e32 v71, v34, v47
	v_cndmask_b32_e32 v20, 0, v20, vcc
	v_cndmask_b32_e32 v21, 0, v21, vcc
	v_cndmask_b32_e32 v34, 0, v97, vcc
	v_add_f32_e32 v48, v56, v48
	v_add_f32_e32 v68, v44, v36
	v_add_f32_e32 v69, v35, v43
	v_add_f32_e32 v50, v50, v34
	v_add_f32_e32 v72, v21, v18
	v_add_f32_e32 v73, v20, v19
	v_add_f32_e32 v52, v48, v37
	ds_write_b128 v1, v[26:29] offset:24576
	v_add_co_u32_e32 v18, vcc, s10, v130
	s_mov_b32 s11, 0xc8c000
	s_nop 0
	v_addc_co_u32_e32 v19, vcc, 0, v131, vcc
	v_add_co_u32_e32 v20, vcc, s11, v130
	s_mov_b32 s11, 0x190c000
	s_nop 0
	v_addc_co_u32_e32 v21, vcc, 0, v131, vcc
	global_load_dwordx4 v[54:57], v[18:19], off sc0 nt
	global_load_dwordx4 v[42:45], v[20:21], off sc0 nt
	v_add_co_u32_e32 v18, vcc, s11, v130
	s_mov_b32 s11, 0x258c000
	s_nop 0
	v_addc_co_u32_e32 v19, vcc, 0, v131, vcc
	v_add_co_u32_e32 v20, vcc, s11, v130
	s_mov_b32 s11, 0x320c000
	s_nop 0
	v_addc_co_u32_e32 v21, vcc, 0, v131, vcc
	global_load_dwordx4 v[46:49], v[18:19], off sc0 nt
	global_load_dwordx4 v[26:29], v[20:21], off sc0 nt
	v_add_co_u32_e32 v18, vcc, s11, v130
	v_add_u32_e32 v74, 0x900, v137
	s_nop 0
	v_addc_co_u32_e32 v19, vcc, 0, v131, vcc
	global_load_dwordx4 v[34:37], v[18:19], off sc0 nt
	v_add_co_u32_e32 v18, vcc, s10, v132
	s_waitcnt vmcnt(10)
	v_mul_f32_e32 v62, 0x4038aa3b, v62
	v_addc_co_u32_e32 v19, vcc, 0, v133, vcc
	global_load_dwordx4 v[18:21], v[18:19], off sc0 nt
	s_waitcnt vmcnt(10)
	v_mul_f32_e32 v38, 0x4038aa3b, v38
	s_waitcnt vmcnt(9)
	v_mul_f32_e32 v58, 0x4038aa3b, v58
	v_mul_u32_u24_sdwa v100, v74, s6 dst_sel:DWORD dst_unused:UNUSED_PAD src0_sel:WORD_0 src1_sel:DWORD
	v_exp_f32_e32 v62, v62
	v_exp_f32_e32 v38, v38
	v_exp_f32_e32 v58, v58
	v_lshrrev_b32_e32 v100, 23, v100
	v_cvt_f32_u32_e32 v101, v100
	v_mul_i32_i24_e32 v100, 0xffffff60, v100
	v_add_lshl_u32 v74, v100, v74, 2
	v_cvt_f32_i32_e32 v74, v74
	v_add_f32_e32 v62, 1.0, v62
	v_add_f32_e32 v38, 1.0, v38
	v_add_f32_e32 v58, 1.0, v58
	v_rcp_f32_e32 v62, v62
	v_rcp_f32_e32 v38, v38
	v_rcp_f32_e32 v58, v58
	v_mul_f32_e32 v63, 0x4038aa3b, v63
	v_mul_f32_e32 v39, 0x4038aa3b, v39
	v_mul_f32_e32 v59, 0x4038aa3b, v59
	v_fma_f32 v108, v101, s7, 1.0
	v_fma_f32 v74, v74, s9, 1.0
	v_exp_f32_e32 v63, v63
	v_exp_f32_e32 v39, v39
	v_exp_f32_e32 v59, v59
	v_fma_f32 v62, -2.0, v62, v128
	v_fma_f32 v38, -2.0, v38, v108
	v_fma_f32 v58, -2.0, v58, v74
	v_add_f32_e32 v100, v62, v38
	v_mul_f32_e32 v102, v58, v58
	s_waitcnt vmcnt(6)
	v_cmp_eq_u32_e32 vcc, 1, v14
	v_add_f32_e32 v100, v100, v58
	v_fmac_f32_e32 v102, v38, v38
	v_mul_f32_e32 v38, v22, v22
	v_cndmask_b32_e64 v58, 0, 1.0, vcc
	v_fmac_f32_e32 v102, v62, v62
	v_add_f32_e32 v51, v51, v58
	v_cndmask_b32_e32 v58, 0, v38, vcc
	v_cndmask_b32_e32 v62, 0, v22, vcc
	v_cndmask_b32_e32 v101, 0, v100, vcc
	v_cmp_eq_u32_e32 vcc, 2, v14
	v_add_f32_e32 v63, 1.0, v63
	v_add_f32_e32 v39, 1.0, v39
	v_add_f32_e32 v59, 1.0, v59
	v_add_f32_e32 v53, v53, v62
	v_cndmask_b32_e64 v62, 0, 1.0, vcc
	v_rcp_f32_e32 v63, v63
	v_rcp_f32_e32 v39, v39
	v_rcp_f32_e32 v59, v59
	v_add_f32_e32 v52, v52, v101
	v_add_f32_e32 v58, v66, v58
	v_add_f32_e32 v62, v67, v62
	v_cndmask_b32_e32 v66, 0, v38, vcc
	v_cndmask_b32_e32 v67, 0, v22, vcc
	v_cndmask_b32_e32 v101, 0, v100, vcc
	v_cmp_eq_u32_e32 vcc, 3, v14
	v_add_f32_e32 v66, v70, v66
	v_fma_f32 v63, -2.0, v63, v128
	v_cndmask_b32_e32 v70, 0, v100, vcc
	v_add_f32_e32 v50, v50, v70
	v_add_f32_e32 v70, 0x3b086211, v74
	v_fma_f32 v39, -2.0, v39, v108
	v_fmac_f32_e32 v70, -2.0, v59
	v_add_f32_e32 v67, v69, v67
	v_cndmask_b32_e64 v69, 0, 1.0, vcc
	v_cndmask_b32_e32 v38, 0, v38, vcc
	v_cndmask_b32_e32 v22, 0, v22, vcc
	v_add_f32_e32 v59, v63, v39
	v_mul_f32_e32 v103, v70, v70
	v_cmp_eq_u32_e32 vcc, 1, v15
	v_add_f32_e32 v68, v68, v101
	v_add_f32_e32 v101, v59, v70
	v_fmac_f32_e32 v103, v39, v39
	v_mul_f32_e32 v39, v23, v23
	v_cndmask_b32_e64 v59, 0, 1.0, vcc
	v_fmac_f32_e32 v103, v63, v63
	v_add_f32_e32 v51, v59, v51
	v_cndmask_b32_e32 v59, 0, v39, vcc
	v_cndmask_b32_e32 v63, 0, v23, vcc
	v_cndmask_b32_e32 v70, 0, v101, vcc
	v_cmp_eq_u32_e32 vcc, 2, v15
	v_add_f32_e32 v58, v59, v58
	v_add_f32_e32 v52, v52, v70
	v_cndmask_b32_e64 v59, 0, 1.0, vcc
	v_add_f32_e32 v53, v63, v53
	v_add_f32_e32 v59, v59, v62
	v_cndmask_b32_e32 v62, 0, v39, vcc
	v_cndmask_b32_e32 v63, 0, v23, vcc
	v_cndmask_b32_e32 v70, 0, v101, vcc
	v_cmp_eq_u32_e32 vcc, 3, v15
	v_add_f32_e32 v22, v72, v22
	v_add_f32_e32 v38, v73, v38
	v_cndmask_b32_e32 v39, 0, v39, vcc
	v_cndmask_b32_e32 v23, 0, v23, vcc
	v_add_f32_e32 v22, v23, v22
	v_add_f32_e32 v23, v39, v38
	v_mul_f32_e32 v39, 0x4038aa3b, v40
	v_mul_f32_e32 v40, 0x4038aa3b, v60
	v_mul_f32_e32 v64, 0x4038aa3b, v64
	v_exp_f32_e32 v40, v40
	v_exp_f32_e32 v64, v64
	v_exp_f32_e32 v39, v39
	v_add_f32_e32 v60, 0x3b886211, v74
	v_add_f32_e32 v40, 1.0, v40
	v_add_f32_e32 v38, 1.0, v64
	v_add_f32_e32 v39, 1.0, v39
	v_rcp_f32_e32 v40, v40
	v_rcp_f32_e32 v38, v38
	v_rcp_f32_e32 v39, v39
	v_add_f32_e32 v63, v63, v67
	v_fmac_f32_e32 v60, -2.0, v40
	v_fma_f32 v38, -2.0, v38, v128
	v_fma_f32 v39, -2.0, v39, v108
	v_mul_f32_e32 v106, v60, v60
	v_add_f32_e32 v62, v62, v66
	v_cndmask_b32_e64 v66, 0, 1.0, vcc
	v_cndmask_b32_e32 v67, 0, v101, vcc
	v_add_f32_e32 v40, v38, v39
	v_fmac_f32_e32 v106, v39, v39
	v_cmp_eq_u32_e32 vcc, 1, v16
	v_add_f32_e32 v104, v40, v60
	v_fmac_f32_e32 v106, v38, v38
	v_mul_f32_e32 v38, v24, v24
	v_cndmask_b32_e64 v39, 0, 1.0, vcc
	v_add_f32_e32 v39, v39, v51
	v_cndmask_b32_e32 v40, 0, v38, vcc
	v_cndmask_b32_e32 v51, 0, v24, vcc
	v_cndmask_b32_e32 v60, 0, v104, vcc
	v_cmp_eq_u32_e32 vcc, 2, v16
	v_add_f32_e32 v51, v51, v53
	v_add_f32_e32 v52, v52, v60
	v_cndmask_b32_e64 v53, 0, 1.0, vcc
	v_add_f32_e32 v40, v40, v58
	v_add_f32_e32 v53, v53, v59
	v_cndmask_b32_e32 v58, 0, v38, vcc
	v_cndmask_b32_e32 v59, 0, v24, vcc
	v_cndmask_b32_e32 v60, 0, v104, vcc
	v_cmp_eq_u32_e32 vcc, 3, v16
	v_mul_f32_e32 v64, 0x4038aa3b, v65
	v_exp_f32_e32 v64, v64
	v_cndmask_b32_e32 v38, 0, v38, vcc
	v_add_f32_e32 v23, v38, v23
	v_mul_f32_e32 v38, 0x4038aa3b, v41
	v_mul_f32_e32 v41, 0x4038aa3b, v61
	v_exp_f32_e32 v41, v41
	v_exp_f32_e32 v38, v38
	v_cndmask_b32_e32 v24, 0, v24, vcc
	v_add_f32_e32 v22, v24, v22
	v_add_f32_e32 v41, 1.0, v41
	v_add_f32_e32 v38, 1.0, v38
	v_rcp_f32_e32 v41, v41
	v_add_f32_e32 v24, 1.0, v64
	v_rcp_f32_e32 v38, v38
	v_rcp_f32_e32 v24, v24
	v_mul_f32_e32 v33, 0xbfb8aa3b, v33
	v_add_f32_e32 v61, 0x3bcc931a, v74
	v_exp_f32_e32 v33, v33
	v_fmac_f32_e32 v61, -2.0, v41
	v_mul_f32_e32 v30, 0xbfb8aa3b, v30
	v_mul_f32_e32 v31, 0xbfb8aa3b, v31
	v_mul_f32_e32 v32, 0xbfb8aa3b, v32
	v_fmac_f32_e32 v108, -2.0, v38
	v_mul_f32_e32 v107, v61, v61
	v_exp_f32_e32 v30, v30
	v_exp_f32_e32 v31, v31
	v_exp_f32_e32 v32, v32
	v_fma_f32 v24, -2.0, v24, v128
	v_fmac_f32_e32 v107, v108, v108
	v_add_f32_e32 v59, v59, v63
	v_add_f32_e32 v58, v58, v62
	v_cndmask_b32_e64 v62, 0, 1.0, vcc
	v_cndmask_b32_e32 v63, 0, v104, vcc
	v_add_f32_e32 v38, v24, v108
	v_fmac_f32_e32 v107, v24, v24
	v_add_f32_e32 v24, 1.0, v33
	v_cmp_eq_u32_e32 vcc, 1, v17
	v_add_f32_e32 v105, v38, v61
	v_rcp_f32_e32 v33, v24
	v_mul_f32_e32 v24, v25, v25
	v_cndmask_b32_e64 v38, 0, 1.0, vcc
	v_add_f32_e32 v61, v38, v39
	v_cndmask_b32_e32 v38, 0, v24, vcc
	v_cndmask_b32_e32 v39, 0, v25, vcc
	v_cndmask_b32_e32 v41, 0, v105, vcc
	v_cmp_eq_u32_e32 vcc, 2, v17
	v_add_f32_e32 v30, 1.0, v30
	v_add_f32_e32 v69, v71, v69
	v_add_f32_e32 v31, 1.0, v31
	v_add_f32_e32 v32, 1.0, v32
	v_add_f32_e32 v72, v38, v40
	v_cndmask_b32_e64 v38, 0, 1.0, vcc
	v_rcp_f32_e32 v30, v30
	v_rcp_f32_e32 v31, v31
	v_add_f32_e32 v66, v66, v69
	v_rcp_f32_e32 v32, v32
	v_add_f32_e32 v71, v39, v51
	v_add_f32_e32 v73, v38, v53
	v_cndmask_b32_e32 v38, 0, v24, vcc
	v_cndmask_b32_e32 v39, 0, v25, vcc
	v_cndmask_b32_e32 v40, 0, v105, vcc
	v_cmp_eq_u32_e32 vcc, 3, v17
	v_add_f32_e32 v68, v68, v70
	v_add_f32_e32 v50, v50, v67
	v_add_f32_e32 v62, v62, v66
	v_add_f32_e32 v58, v38, v58
	v_cndmask_b32_e64 v38, 0, 1.0, vcc
	v_add_f32_e32 v60, v68, v60
	v_add_f32_e32 v50, v50, v63
	v_add_f32_e32 v74, v38, v62
	v_cndmask_b32_e32 v24, 0, v24, vcc
	v_cndmask_b32_e32 v25, 0, v25, vcc
	v_cndmask_b32_e32 v38, 0, v105, vcc
	v_add_f32_e32 v70, v52, v41
	v_add_f32_e32 v60, v60, v40
	v_add_f32_e32 v59, v39, v59
	v_add_f32_e32 v109, v50, v38
	v_add_f32_e32 v111, v25, v22
	v_add_f32_e32 v112, v24, v23
	ds_write_b128 v1, v[30:33] offset:36864
	s_mov_b32 s10, 0xf000
	v_add_co_u32_e32 v22, vcc, s10, v130
	s_mov_b32 s11, 0xc8f000
	s_nop 0
	v_addc_co_u32_e32 v23, vcc, 0, v131, vcc
	v_add_co_u32_e32 v24, vcc, s11, v130
	s_mov_b32 s11, 0x190f000
	s_nop 0
	v_addc_co_u32_e32 v25, vcc, 0, v131, vcc
	global_load_dwordx4 v[66:69], v[22:23], off sc0 nt
	global_load_dwordx4 v[50:53], v[24:25], off sc0 nt
	v_add_co_u32_e32 v22, vcc, s11, v130
	s_mov_b32 s11, 0x258f000
	s_nop 0
	v_addc_co_u32_e32 v23, vcc, 0, v131, vcc
	v_add_co_u32_e32 v24, vcc, s11, v130
	s_mov_b32 s11, 0x320f000
	s_nop 0
	v_addc_co_u32_e32 v25, vcc, 0, v131, vcc
	global_load_dwordx4 v[62:65], v[22:23], off sc0 nt
	global_load_dwordx4 v[30:33], v[24:25], off sc0 nt
	v_add_co_u32_e32 v22, vcc, s11, v130
	v_or_b32_e32 v116, 0xc00, v0
	s_nop 0
	v_addc_co_u32_e32 v23, vcc, 0, v131, vcc
	global_load_dwordx4 v[38:41], v[22:23], off sc0 nt
	v_add_co_u32_e32 v22, vcc, s10, v132
	v_add_u32_e32 v108, s8, v116
	s_nop 0
	v_addc_co_u32_e32 v23, vcc, 0, v133, vcc
	global_load_dwordx4 v[22:25], v[22:23], off sc0 nt
	s_waitcnt vmcnt(11)
	v_mul_f32_e32 v54, 0x4038aa3b, v54
	s_waitcnt vmcnt(10)
	v_mul_f32_e32 v42, 0x4038aa3b, v42
	s_waitcnt vmcnt(9)
	v_mul_f32_e32 v46, 0x4038aa3b, v46
	v_mul_u32_u24_sdwa v110, v108, s6 dst_sel:DWORD dst_unused:UNUSED_PAD src0_sel:WORD_0 src1_sel:DWORD
	v_exp_f32_e32 v54, v54
	v_exp_f32_e32 v42, v42
	v_exp_f32_e32 v46, v46
	v_lshrrev_b32_e32 v110, 23, v110
	v_cvt_f32_u32_e32 v113, v110
	v_mul_i32_i24_e32 v110, 0xffffff60, v110
	v_add_lshl_u32 v108, v110, v108, 2
	v_cvt_f32_i32_e32 v108, v108
	v_add_f32_e32 v54, 1.0, v54
	v_add_f32_e32 v42, 1.0, v42
	v_add_f32_e32 v46, 1.0, v46
	v_rcp_f32_e32 v54, v54
	v_rcp_f32_e32 v42, v42
	v_rcp_f32_e32 v46, v46
	v_mul_f32_e32 v55, 0x4038aa3b, v55
	v_mul_f32_e32 v43, 0x4038aa3b, v43
	v_mul_f32_e32 v47, 0x4038aa3b, v47
	v_fma_f32 v117, v113, s7, 1.0
	v_fma_f32 v113, v108, s9, 1.0
	v_exp_f32_e32 v55, v55
	v_exp_f32_e32 v43, v43
	v_exp_f32_e32 v47, v47
	v_fma_f32 v54, -2.0, v54, v128
	v_fma_f32 v42, -2.0, v42, v117
	v_fma_f32 v46, -2.0, v46, v113
	v_add_f32_e32 v108, v54, v42
	v_mul_f32_e32 v110, v46, v46
	s_waitcnt vmcnt(6)
	v_cmp_eq_u32_e32 vcc, 1, v18
	v_add_f32_e32 v108, v108, v46
	v_fmac_f32_e32 v110, v42, v42
	v_mul_f32_e32 v42, v26, v26
	v_cndmask_b32_e64 v46, 0, 1.0, vcc
	v_fmac_f32_e32 v110, v54, v54
	v_add_f32_e32 v46, v61, v46
	v_cndmask_b32_e32 v54, 0, v42, vcc
	v_cndmask_b32_e32 v61, 0, v26, vcc
	v_cndmask_b32_e32 v114, 0, v108, vcc
	v_cmp_eq_u32_e32 vcc, 2, v18
	v_add_f32_e32 v55, 1.0, v55
	v_add_f32_e32 v43, 1.0, v43
	v_add_f32_e32 v47, 1.0, v47
	v_add_f32_e32 v61, v71, v61
	v_cndmask_b32_e64 v71, 0, 1.0, vcc
	v_rcp_f32_e32 v55, v55
	v_rcp_f32_e32 v43, v43
	v_rcp_f32_e32 v47, v47
	v_add_f32_e32 v70, v70, v114
	v_add_f32_e32 v54, v72, v54
	v_add_f32_e32 v71, v73, v71
	v_cndmask_b32_e32 v72, 0, v42, vcc
	v_cndmask_b32_e32 v73, 0, v26, vcc
	v_cndmask_b32_e32 v114, 0, v108, vcc
	v_cmp_eq_u32_e32 vcc, 3, v18
	v_add_f32_e32 v58, v58, v72
	v_fma_f32 v55, -2.0, v55, v128
	v_cndmask_b32_e64 v72, 0, 1.0, vcc
	v_add_f32_e32 v72, v74, v72
	v_add_f32_e32 v74, 0x3b086211, v113
	v_cndmask_b32_e32 v26, 0, v26, vcc
	v_fma_f32 v43, -2.0, v43, v117
	v_fmac_f32_e32 v74, -2.0, v47
	v_add_f32_e32 v59, v59, v73
	v_cndmask_b32_e32 v42, 0, v42, vcc
	v_cndmask_b32_e32 v73, 0, v108, vcc
	v_add_f32_e32 v26, v111, v26
	v_add_f32_e32 v47, v55, v43
	v_mul_f32_e32 v111, v74, v74
	v_cmp_eq_u32_e32 vcc, 1, v19
	v_add_f32_e32 v73, v109, v73
	v_add_f32_e32 v109, v47, v74
	v_fmac_f32_e32 v111, v43, v43
	v_mul_f32_e32 v43, v27, v27
	v_cndmask_b32_e64 v47, 0, 1.0, vcc
	v_fmac_f32_e32 v111, v55, v55
	v_add_f32_e32 v46, v47, v46
	v_cndmask_b32_e32 v47, 0, v43, vcc
	v_cndmask_b32_e32 v55, 0, v27, vcc
	v_cndmask_b32_e32 v74, 0, v109, vcc
	v_cmp_eq_u32_e32 vcc, 2, v19
	v_add_f32_e32 v47, v47, v54
	v_add_f32_e32 v70, v70, v74
	v_cndmask_b32_e64 v54, 0, 1.0, vcc
	v_add_f32_e32 v55, v55, v61
	v_add_f32_e32 v54, v54, v71
	v_cndmask_b32_e32 v61, 0, v43, vcc
	v_cndmask_b32_e32 v71, 0, v27, vcc
	v_cndmask_b32_e32 v74, 0, v109, vcc
	v_cmp_eq_u32_e32 vcc, 3, v19
	v_add_f32_e32 v42, v112, v42
	v_mul_f32_e32 v56, 0x4038aa3b, v56
	v_cndmask_b32_e32 v43, 0, v43, vcc
	v_cndmask_b32_e32 v27, 0, v27, vcc
	v_add_f32_e32 v26, v27, v26
	v_add_f32_e32 v27, v43, v42
	v_mul_f32_e32 v43, 0x4038aa3b, v44
	v_mul_f32_e32 v44, 0x4038aa3b, v48
	v_exp_f32_e32 v44, v44
	v_exp_f32_e32 v56, v56
	v_exp_f32_e32 v43, v43
	v_add_f32_e32 v48, 0x3b886211, v113
	v_add_f32_e32 v44, 1.0, v44
	v_add_f32_e32 v42, 1.0, v56
	v_add_f32_e32 v43, 1.0, v43
	v_rcp_f32_e32 v44, v44
	v_rcp_f32_e32 v42, v42
	v_rcp_f32_e32 v43, v43
	v_add_f32_e32 v60, v60, v114
	v_fmac_f32_e32 v48, -2.0, v44
	v_fma_f32 v42, -2.0, v42, v128
	v_fma_f32 v43, -2.0, v43, v117
	v_mul_f32_e32 v114, v48, v48
	v_add_f32_e32 v59, v71, v59
	v_add_f32_e32 v58, v61, v58
	v_cndmask_b32_e64 v61, 0, 1.0, vcc
	v_cndmask_b32_e32 v71, 0, v109, vcc
	v_add_f32_e32 v44, v42, v43
	v_fmac_f32_e32 v114, v43, v43
	v_cmp_eq_u32_e32 vcc, 1, v20
	v_add_f32_e32 v112, v44, v48
	v_fmac_f32_e32 v114, v42, v42
	v_mul_f32_e32 v42, v28, v28
	v_cndmask_b32_e64 v43, 0, 1.0, vcc
	v_add_f32_e32 v43, v43, v46
	v_cndmask_b32_e32 v44, 0, v42, vcc
	v_cndmask_b32_e32 v46, 0, v28, vcc
	v_cndmask_b32_e32 v48, 0, v112, vcc
	v_cmp_eq_u32_e32 vcc, 2, v20
	v_add_f32_e32 v44, v44, v47
	v_add_f32_e32 v46, v46, v55
	v_cndmask_b32_e64 v47, 0, 1.0, vcc
	v_add_f32_e32 v47, v47, v54
	v_cndmask_b32_e32 v54, 0, v42, vcc
	v_cndmask_b32_e32 v55, 0, v28, vcc
	v_cndmask_b32_e32 v56, 0, v112, vcc
	v_cmp_eq_u32_e32 vcc, 3, v20
	v_mul_f32_e32 v57, 0x4038aa3b, v57
	v_exp_f32_e32 v57, v57
	v_cndmask_b32_e32 v42, 0, v42, vcc
	v_add_f32_e32 v27, v42, v27
	v_mul_f32_e32 v42, 0x4038aa3b, v45
	v_mul_f32_e32 v45, 0x4038aa3b, v49
	v_exp_f32_e32 v45, v45
	v_exp_f32_e32 v42, v42
	v_cndmask_b32_e32 v28, 0, v28, vcc
	v_add_f32_e32 v26, v28, v26
	v_add_f32_e32 v45, 1.0, v45
	v_add_f32_e32 v42, 1.0, v42
	v_rcp_f32_e32 v45, v45
	v_add_f32_e32 v28, 1.0, v57
	v_rcp_f32_e32 v42, v42
	v_rcp_f32_e32 v28, v28
	v_mul_f32_e32 v37, 0xbfb8aa3b, v37
	v_add_f32_e32 v49, 0x3bcc931a, v113
	v_exp_f32_e32 v37, v37
	v_fmac_f32_e32 v49, -2.0, v45
	v_mul_f32_e32 v34, 0xbfb8aa3b, v34
	v_mul_f32_e32 v35, 0xbfb8aa3b, v35
	v_mul_f32_e32 v36, 0xbfb8aa3b, v36
	v_fmac_f32_e32 v117, -2.0, v42
	v_mul_f32_e32 v115, v49, v49
	v_exp_f32_e32 v34, v34
	v_exp_f32_e32 v35, v35
	v_exp_f32_e32 v36, v36
	v_fma_f32 v28, -2.0, v28, v128
	v_fmac_f32_e32 v115, v117, v117
	v_add_f32_e32 v55, v55, v59
	v_add_f32_e32 v54, v54, v58
	v_cndmask_b32_e64 v58, 0, 1.0, vcc
	v_cndmask_b32_e32 v59, 0, v112, vcc
	v_add_f32_e32 v42, v28, v117
	v_fmac_f32_e32 v115, v28, v28
	v_add_f32_e32 v28, 1.0, v37
	v_cmp_eq_u32_e32 vcc, 1, v21
	v_add_f32_e32 v113, v42, v49
	v_rcp_f32_e32 v37, v28
	v_mul_f32_e32 v28, v29, v29
	v_cndmask_b32_e64 v42, 0, 1.0, vcc
	v_add_f32_e32 v48, v70, v48
	v_add_f32_e32 v70, v42, v43
	v_cndmask_b32_e32 v42, 0, v28, vcc
	v_cndmask_b32_e32 v43, 0, v29, vcc
	v_cndmask_b32_e32 v45, 0, v113, vcc
	v_cmp_eq_u32_e32 vcc, 2, v21
	v_add_f32_e32 v34, 1.0, v34
	v_add_f32_e32 v35, 1.0, v35
	v_add_f32_e32 v71, v73, v71
	v_add_f32_e32 v36, 1.0, v36
	v_add_f32_e32 v73, v42, v44
	v_cndmask_b32_e64 v42, 0, 1.0, vcc
	v_rcp_f32_e32 v34, v34
	v_rcp_f32_e32 v35, v35
	v_add_f32_e32 v60, v60, v74
	v_add_f32_e32 v61, v61, v72
	v_rcp_f32_e32 v36, v36
	v_add_f32_e32 v72, v43, v46
	v_add_f32_e32 v74, v42, v47
	v_cndmask_b32_e32 v42, 0, v28, vcc
	v_cndmask_b32_e32 v43, 0, v29, vcc
	v_cndmask_b32_e32 v44, 0, v113, vcc
	v_cmp_eq_u32_e32 vcc, 3, v21
	v_add_f32_e32 v58, v58, v61
	v_add_f32_e32 v120, v42, v54
	v_cndmask_b32_e64 v42, 0, 1.0, vcc
	v_add_f32_e32 v56, v60, v56
	v_add_f32_e32 v59, v71, v59
	v_add_f32_e32 v121, v42, v58
	v_cndmask_b32_e32 v28, 0, v28, vcc
	v_cndmask_b32_e32 v29, 0, v29, vcc
	v_cndmask_b32_e32 v42, 0, v113, vcc
	v_add_f32_e32 v71, v48, v45
	v_add_f32_e32 v117, v56, v44
	v_add_f32_e32 v119, v43, v55
	v_add_f32_e32 v122, v59, v42
	v_add_f32_e32 v123, v29, v26
	v_add_f32_e32 v124, v28, v27
	v_lshl_add_u32 v26, v116, 4, v136
	ds_write_b128 v26, v[34:37] offset:49152
	s_mov_b32 s10, 0x12000
	v_add_co_u32_e32 v26, vcc, s10, v130
	s_mov_b32 s11, 0xc92000
	s_nop 0
	v_addc_co_u32_e32 v27, vcc, 0, v131, vcc
	v_add_co_u32_e32 v28, vcc, s11, v130
	s_mov_b32 s11, 0x1912000
	s_nop 0
	v_addc_co_u32_e32 v29, vcc, 0, v131, vcc
	global_load_dwordx4 v[58:61], v[26:27], off sc0 nt
	global_load_dwordx4 v[46:49], v[28:29], off sc0 nt
	v_add_co_u32_e32 v26, vcc, s11, v130
	s_mov_b32 s11, 0x2592000
	s_nop 0
	v_addc_co_u32_e32 v27, vcc, 0, v131, vcc
	v_add_co_u32_e32 v28, vcc, s11, v130
	s_mov_b32 s11, 0x3212000
	s_nop 0
	v_addc_co_u32_e32 v29, vcc, 0, v131, vcc
	global_load_dwordx4 v[54:57], v[26:27], off sc0 nt
	global_load_dwordx4 v[34:37], v[28:29], off sc0 nt
	v_add_co_u32_e32 v26, vcc, s11, v130
	v_add_u32_e32 v116, 0xf00, v137
	s_nop 0
	v_addc_co_u32_e32 v27, vcc, 0, v131, vcc
	global_load_dwordx4 v[42:45], v[26:27], off sc0 nt
	v_add_co_u32_e32 v26, vcc, s10, v132
	s_waitcnt vmcnt(10)
	v_mul_f32_e32 v66, 0x4038aa3b, v66
	v_addc_co_u32_e32 v27, vcc, 0, v133, vcc
	global_load_dwordx4 v[26:29], v[26:27], off sc0 nt
	s_waitcnt vmcnt(10)
	v_mul_f32_e32 v50, 0x4038aa3b, v50
	s_waitcnt vmcnt(9)
	v_mul_f32_e32 v62, 0x4038aa3b, v62
	v_mul_u32_u24_sdwa v118, v116, s6 dst_sel:DWORD dst_unused:UNUSED_PAD src0_sel:WORD_0 src1_sel:DWORD
	v_exp_f32_e32 v66, v66
	v_exp_f32_e32 v50, v50
	v_exp_f32_e32 v62, v62
	v_lshrrev_b32_e32 v118, 23, v118
	v_cvt_f32_u32_e32 v125, v118
	v_mul_i32_i24_e32 v118, 0xffffff60, v118
	v_add_lshl_u32 v116, v118, v116, 2
	v_cvt_f32_i32_e32 v116, v116
	v_add_f32_e32 v66, 1.0, v66
	v_add_f32_e32 v50, 1.0, v50
	v_add_f32_e32 v62, 1.0, v62
	v_rcp_f32_e32 v66, v66
	v_rcp_f32_e32 v50, v50
	v_rcp_f32_e32 v62, v62
	v_mul_f32_e32 v67, 0x4038aa3b, v67
	v_mul_f32_e32 v51, 0x4038aa3b, v51
	v_exp_f32_e32 v67, v67
	v_exp_f32_e32 v51, v51
	v_mul_f32_e32 v63, 0x4038aa3b, v63
	v_exp_f32_e32 v63, v63
	v_fma_f32 v125, v125, s7, 1.0
	v_fma_f32 v126, v116, s9, 1.0
	v_fma_f32 v66, -2.0, v66, v128
	v_fma_f32 v50, -2.0, v50, v125
	v_fma_f32 v62, -2.0, v62, v126
	v_add_f32_e32 v116, v66, v50
	v_mul_f32_e32 v118, v62, v62
	s_waitcnt vmcnt(6)
	v_cmp_eq_u32_e32 vcc, 1, v22
	v_add_f32_e32 v67, 1.0, v67
	v_add_f32_e32 v51, 1.0, v51
	v_add_f32_e32 v116, v116, v62
	v_fmac_f32_e32 v118, v50, v50
	v_mul_f32_e32 v50, v30, v30
	v_cndmask_b32_e64 v62, 0, 1.0, vcc
	v_rcp_f32_e32 v67, v67
	v_rcp_f32_e32 v51, v51
	v_add_f32_e32 v63, 1.0, v63
	v_fmac_f32_e32 v118, v66, v66
	v_add_f32_e32 v62, v70, v62
	v_cndmask_b32_e32 v66, 0, v50, vcc
	v_cndmask_b32_e32 v70, 0, v30, vcc
	v_cndmask_b32_e32 v127, 0, v116, vcc
	v_cmp_eq_u32_e32 vcc, 2, v22
	v_rcp_f32_e32 v63, v63
	v_add_f32_e32 v70, v72, v70
	v_cndmask_b32_e64 v72, 0, 1.0, vcc
	v_add_f32_e32 v71, v71, v127
	v_add_f32_e32 v66, v73, v66
	v_add_f32_e32 v72, v74, v72
	v_cndmask_b32_e32 v73, 0, v50, vcc
	v_cndmask_b32_e32 v74, 0, v30, vcc
	v_cndmask_b32_e32 v127, 0, v116, vcc
	v_cmp_eq_u32_e32 vcc, 3, v22
	v_add_f32_e32 v127, v117, v127
	v_add_f32_e32 v74, v119, v74
	v_cndmask_b32_e64 v117, 0, 1.0, vcc
	v_add_f32_e32 v119, 0x3b086211, v126
	v_fma_f32 v67, -2.0, v67, v128
	v_fma_f32 v51, -2.0, v51, v125
	v_add_f32_e32 v73, v120, v73
	v_add_f32_e32 v120, v121, v117
	v_cndmask_b32_e32 v117, 0, v116, vcc
	v_fmac_f32_e32 v119, -2.0, v63
	v_add_f32_e32 v63, v67, v51
	v_cndmask_b32_e32 v50, 0, v50, vcc
	v_cndmask_b32_e32 v30, 0, v30, vcc
	v_add_f32_e32 v121, v122, v117
	v_add_f32_e32 v117, v63, v119
	v_mul_f32_e32 v119, v119, v119
	v_cmp_eq_u32_e32 vcc, 1, v23
	v_fmac_f32_e32 v119, v51, v51
	v_mul_f32_e32 v51, v31, v31
	v_cndmask_b32_e64 v63, 0, 1.0, vcc
	v_fmac_f32_e32 v119, v67, v67
	v_add_f32_e32 v62, v63, v62
	v_cndmask_b32_e32 v63, 0, v51, vcc
	v_cndmask_b32_e32 v67, 0, v31, vcc
	v_cndmask_b32_e32 v122, 0, v117, vcc
	v_cmp_eq_u32_e32 vcc, 2, v23
	v_add_f32_e32 v63, v63, v66
	v_add_f32_e32 v71, v71, v122
	v_cndmask_b32_e64 v66, 0, 1.0, vcc
	v_add_f32_e32 v67, v67, v70
	v_add_f32_e32 v66, v66, v72
	v_cndmask_b32_e32 v70, 0, v51, vcc
	v_cndmask_b32_e32 v72, 0, v31, vcc
	v_cndmask_b32_e32 v122, 0, v117, vcc
	v_cmp_eq_u32_e32 vcc, 3, v23
	v_add_f32_e32 v30, v123, v30
	v_add_f32_e32 v50, v124, v50
	v_cndmask_b32_e32 v51, 0, v51, vcc
	v_cndmask_b32_e32 v31, 0, v31, vcc
	v_add_f32_e32 v30, v31, v30
	v_add_f32_e32 v31, v51, v50
	v_mul_f32_e32 v51, 0x4038aa3b, v52
	v_mul_f32_e32 v52, 0x4038aa3b, v64
	v_mul_f32_e32 v68, 0x4038aa3b, v68
	v_exp_f32_e32 v52, v52
	v_exp_f32_e32 v68, v68
	v_exp_f32_e32 v51, v51
	v_add_f32_e32 v64, 0x3b886211, v126
	v_add_f32_e32 v52, 1.0, v52
	v_add_f32_e32 v50, 1.0, v68
	v_add_f32_e32 v51, 1.0, v51
	v_rcp_f32_e32 v52, v52
	v_rcp_f32_e32 v50, v50
	v_rcp_f32_e32 v51, v51
	v_add_f32_e32 v123, v127, v122
	v_fmac_f32_e32 v64, -2.0, v52
	v_fma_f32 v50, -2.0, v50, v128
	v_fma_f32 v51, -2.0, v51, v125
	v_mul_f32_e32 v122, v64, v64
	v_add_f32_e32 v72, v72, v74
	v_add_f32_e32 v70, v70, v73
	v_cndmask_b32_e64 v73, 0, 1.0, vcc
	v_cndmask_b32_e32 v74, 0, v117, vcc
	v_add_f32_e32 v52, v50, v51
	v_fmac_f32_e32 v122, v51, v51
	v_cmp_eq_u32_e32 vcc, 1, v24
	v_add_f32_e32 v73, v73, v120
	v_add_f32_e32 v120, v52, v64
	v_fmac_f32_e32 v122, v50, v50
	v_mul_f32_e32 v50, v32, v32
	v_cndmask_b32_e64 v51, 0, 1.0, vcc
	v_add_f32_e32 v51, v51, v62
	v_cndmask_b32_e32 v52, 0, v50, vcc
	v_cndmask_b32_e32 v62, 0, v32, vcc
	v_cndmask_b32_e32 v64, 0, v120, vcc
	v_cmp_eq_u32_e32 vcc, 2, v24
	v_add_f32_e32 v52, v52, v63
	v_add_f32_e32 v62, v62, v67
	v_cndmask_b32_e64 v63, 0, 1.0, vcc
	v_add_f32_e32 v63, v63, v66
	v_cndmask_b32_e32 v66, 0, v50, vcc
	v_cndmask_b32_e32 v67, 0, v32, vcc
	v_cndmask_b32_e32 v68, 0, v120, vcc
	v_cmp_eq_u32_e32 vcc, 3, v24
	v_mul_f32_e32 v69, 0x4038aa3b, v69
	v_exp_f32_e32 v69, v69
	v_cndmask_b32_e32 v50, 0, v50, vcc
	v_add_f32_e32 v31, v50, v31
	v_mul_f32_e32 v50, 0x4038aa3b, v53
	v_mul_f32_e32 v53, 0x4038aa3b, v65
	v_exp_f32_e32 v53, v53
	v_exp_f32_e32 v50, v50
	v_cndmask_b32_e32 v32, 0, v32, vcc
	v_add_f32_e32 v30, v32, v30
	v_add_f32_e32 v53, 1.0, v53
	v_add_f32_e32 v50, 1.0, v50
	v_rcp_f32_e32 v53, v53
	v_add_f32_e32 v32, 1.0, v69
	v_rcp_f32_e32 v50, v50
	v_rcp_f32_e32 v32, v32
	v_mul_f32_e32 v41, 0xbfb8aa3b, v41
	v_add_f32_e32 v65, 0x3bcc931a, v126
	v_exp_f32_e32 v41, v41
	v_fmac_f32_e32 v65, -2.0, v53
	v_mul_f32_e32 v38, 0xbfb8aa3b, v38
	v_mul_f32_e32 v39, 0xbfb8aa3b, v39
	v_mul_f32_e32 v40, 0xbfb8aa3b, v40
	v_add_f32_e32 v68, v123, v68
	v_fmac_f32_e32 v125, -2.0, v50
	v_mul_f32_e32 v123, v65, v65
	v_exp_f32_e32 v38, v38
	v_exp_f32_e32 v39, v39
	v_exp_f32_e32 v40, v40
	v_fma_f32 v32, -2.0, v32, v128
	v_fmac_f32_e32 v123, v125, v125
	v_add_f32_e32 v64, v71, v64
	v_add_f32_e32 v66, v66, v70
	v_cndmask_b32_e64 v70, 0, 1.0, vcc
	v_cndmask_b32_e32 v71, 0, v120, vcc
	v_add_f32_e32 v50, v32, v125
	v_fmac_f32_e32 v123, v32, v32
	v_add_f32_e32 v32, 1.0, v41
	v_cmp_eq_u32_e32 vcc, 1, v25
	v_add_f32_e32 v74, v121, v74
	v_add_f32_e32 v121, v50, v65
	v_rcp_f32_e32 v41, v32
	v_mul_f32_e32 v32, v33, v33
	v_cndmask_b32_e64 v50, 0, 1.0, vcc
	v_add_f32_e32 v71, v74, v71
	v_add_f32_e32 v74, v50, v51
	v_cndmask_b32_e32 v50, 0, v32, vcc
	v_cndmask_b32_e32 v51, 0, v33, vcc
	v_cndmask_b32_e32 v53, 0, v121, vcc
	v_cmp_eq_u32_e32 vcc, 2, v25
	v_add_f32_e32 v38, 1.0, v38
	v_add_f32_e32 v39, 1.0, v39
	v_add_f32_e32 v40, 1.0, v40
	v_add_f32_e32 v139, v50, v52
	v_cndmask_b32_e64 v50, 0, 1.0, vcc
	v_rcp_f32_e32 v38, v38
	v_rcp_f32_e32 v39, v39
	v_rcp_f32_e32 v40, v40
	v_add_f32_e32 v138, v51, v62
	v_add_f32_e32 v140, v50, v63
	v_cndmask_b32_e32 v50, 0, v32, vcc
	v_cndmask_b32_e32 v51, 0, v33, vcc
	v_cndmask_b32_e32 v52, 0, v121, vcc
	v_cmp_eq_u32_e32 vcc, 3, v25
	v_add_f32_e32 v70, v70, v73
	v_add_f32_e32 v143, v50, v66
	v_cndmask_b32_e64 v50, 0, 1.0, vcc
	v_add_f32_e32 v67, v67, v72
	v_add_f32_e32 v144, v50, v70
	v_cndmask_b32_e32 v50, 0, v121, vcc
	v_add_f32_e32 v135, v64, v53
	v_add_f32_e32 v141, v68, v52
	v_add_f32_e32 v142, v51, v67
	v_cndmask_b32_e32 v32, 0, v32, vcc
	v_cndmask_b32_e32 v33, 0, v33, vcc
	v_add_f32_e32 v145, v71, v50
	v_add_f32_e32 v146, v33, v30
	v_add_f32_e32 v147, v32, v31
	ds_write_b128 v1, v[38:41] offset:61440
	s_mov_b32 s10, 0x15000
	v_add_co_u32_e32 v30, vcc, s10, v130
	s_mov_b32 s11, 0xc95000
	s_nop 0
	v_addc_co_u32_e32 v31, vcc, 0, v131, vcc
	v_add_co_u32_e32 v32, vcc, s11, v130
	s_mov_b32 s11, 0x1915000
	s_nop 0
	v_addc_co_u32_e32 v33, vcc, 0, v131, vcc
	global_load_dwordx4 v[70:73], v[30:31], off sc0 nt
	global_load_dwordx4 v[62:65], v[32:33], off sc0 nt
	v_add_co_u32_e32 v30, vcc, s11, v130
	s_mov_b32 s11, 0x2595000
	s_nop 0
	v_addc_co_u32_e32 v31, vcc, 0, v131, vcc
	v_add_co_u32_e32 v32, vcc, s11, v130
	s_mov_b32 s11, 0x3215000
	s_nop 0
	v_addc_co_u32_e32 v33, vcc, 0, v131, vcc
	global_load_dwordx4 v[66:69], v[30:31], off sc0 nt
	global_load_dwordx4 v[38:41], v[32:33], off sc0 nt
	v_add_co_u32_e32 v30, vcc, s11, v130
	s_waitcnt vmcnt(8)
	v_mul_f32_e32 v46, 0x4038aa3b, v46
	v_addc_co_u32_e32 v31, vcc, 0, v131, vcc
	global_load_dwordx4 v[50:53], v[30:31], off sc0 nt
	v_add_co_u32_e32 v30, vcc, s10, v132
	v_add_u32_e32 v124, 0x1200, v137
	s_nop 0
	v_addc_co_u32_e32 v31, vcc, 0, v133, vcc
	v_mul_f32_e32 v58, 0x4038aa3b, v58
	v_exp_f32_e32 v46, v46
	s_waitcnt vmcnt(8)
	v_mul_f32_e32 v54, 0x4038aa3b, v54
	global_load_dwordx4 v[30:33], v[30:31], off sc0 nt
	v_mul_u32_u24_sdwa v125, v124, s6 dst_sel:DWORD dst_unused:UNUSED_PAD src0_sel:WORD_0 src1_sel:DWORD
	v_exp_f32_e32 v58, v58
	v_exp_f32_e32 v54, v54
	v_lshrrev_b32_e32 v125, 23, v125
	v_mul_i32_i24_e32 v126, 0xffffff60, v125
	v_add_lshl_u32 v124, v126, v124, 2
	v_add_f32_e32 v46, 1.0, v46
	v_cvt_f32_u32_e32 v127, v125
	v_cvt_f32_i32_e32 v126, v124
	v_add_f32_e32 v58, 1.0, v58
	v_rcp_f32_e32 v125, v46
	v_add_f32_e32 v46, 1.0, v54
	v_rcp_f32_e32 v124, v58
	v_rcp_f32_e32 v46, v46
	v_fma_f32 v129, v127, s7, 1.0
	v_fma_f32 v54, v126, s9, 1.0
	v_pk_fma_f32 v[126:127], v[124:125], -2.0, v[128:129] op_sel_hi:[1,0,1]
	v_fma_f32 v46, -2.0, v46, v54
	v_add_f32_e32 v58, v126, v127
	v_mul_f32_e32 v124, v46, v46
	s_waitcnt vmcnt(6)
	v_cmp_eq_u32_e32 vcc, 1, v26
	v_add_f32_e32 v58, v58, v46
	v_fmac_f32_e32 v124, v127, v127
	v_mul_f32_e32 v46, v34, v34
	v_cndmask_b32_e64 v125, 0, 1.0, vcc
	v_fmac_f32_e32 v124, v126, v126
	v_add_f32_e32 v74, v74, v125
	v_cndmask_b32_e32 v125, 0, v46, vcc
	v_cndmask_b32_e32 v126, 0, v34, vcc
	v_cndmask_b32_e32 v127, 0, v58, vcc
	v_cmp_eq_u32_e32 vcc, 2, v26
	v_add_f32_e32 v127, v135, v127
	v_add_f32_e32 v135, v139, v125
	v_cndmask_b32_e64 v125, 0, 1.0, vcc
	v_add_f32_e32 v126, v138, v126
	v_add_f32_e32 v138, v140, v125
	v_cndmask_b32_e32 v125, 0, v46, vcc
	v_cndmask_b32_e32 v139, 0, v34, vcc
	v_cndmask_b32_e32 v140, 0, v58, vcc
	v_cmp_eq_u32_e32 vcc, 3, v26
	v_add_f32_e32 v140, v141, v140
	v_add_f32_e32 v141, v143, v125
	v_cndmask_b32_e64 v125, 0, 1.0, vcc
	v_add_f32_e32 v139, v142, v139
	v_add_f32_e32 v142, v144, v125
	v_cndmask_b32_e32 v125, 0, v46, vcc
	v_mul_f32_e32 v46, 0x4038aa3b, v59
	v_mul_f32_e32 v47, 0x4038aa3b, v47
	v_exp_f32_e32 v46, v46
	v_exp_f32_e32 v47, v47
	v_mul_f32_e32 v55, 0x4038aa3b, v55
	v_exp_f32_e32 v55, v55
	v_add_f32_e32 v46, 1.0, v46
	v_add_f32_e32 v47, 1.0, v47
	v_rcp_f32_e32 v46, v46
	v_rcp_f32_e32 v47, v47
	v_add_f32_e32 v55, 1.0, v55
	v_rcp_f32_e32 v55, v55
	v_add_f32_e32 v144, v147, v125
	v_add_f32_e32 v125, 0x3b086211, v54
	v_pk_fma_f32 v[46:47], v[46:47], -2.0, v[128:129] op_sel_hi:[1,0,1]
	v_cndmask_b32_e32 v59, 0, v58, vcc
	v_fmac_f32_e32 v125, -2.0, v55
	v_add_f32_e32 v55, v46, v47
	v_add_f32_e32 v143, v145, v59
	v_add_f32_e32 v59, v55, v125
	v_mul_f32_e32 v125, v125, v125
	v_cndmask_b32_e32 v34, 0, v34, vcc
	v_fmac_f32_e32 v125, v47, v47
	v_cmp_eq_u32_e32 vcc, 1, v27
	v_fmac_f32_e32 v125, v46, v46
	v_mul_f32_e32 v46, v35, v35
	v_cndmask_b32_e64 v47, 0, 1.0, vcc
	v_add_f32_e32 v47, v47, v74
	v_cndmask_b32_e32 v55, 0, v46, vcc
	v_cndmask_b32_e32 v74, 0, v35, vcc
	v_cndmask_b32_e32 v145, 0, v59, vcc
	v_cmp_eq_u32_e32 vcc, 2, v27
	v_add_f32_e32 v74, v74, v126
	v_add_f32_e32 v127, v127, v145
	v_cndmask_b32_e64 v126, 0, 1.0, vcc
	v_add_f32_e32 v55, v55, v135
	v_add_f32_e32 v135, v126, v138
	v_cndmask_b32_e32 v126, 0, v46, vcc
	v_cndmask_b32_e32 v138, 0, v35, vcc
	v_cndmask_b32_e32 v145, 0, v59, vcc
	v_cmp_eq_u32_e32 vcc, 3, v27
	v_add_f32_e32 v138, v138, v139
	v_add_f32_e32 v139, v126, v141
	v_cndmask_b32_e64 v126, 0, 1.0, vcc
	v_add_f32_e32 v34, v146, v34
	v_add_f32_e32 v141, v126, v142
	v_cndmask_b32_e32 v35, 0, v35, vcc
	v_cndmask_b32_e32 v126, 0, v59, vcc
	v_add_f32_e32 v142, v143, v126
	v_add_f32_e32 v143, v35, v34
	v_mul_f32_e32 v35, 0x4038aa3b, v48
	v_mul_f32_e32 v48, 0x4038aa3b, v56
	v_mul_f32_e32 v60, 0x4038aa3b, v60
	v_exp_f32_e32 v48, v48
	v_exp_f32_e32 v60, v60
	v_exp_f32_e32 v35, v35
	v_mul_f32_e32 v44, 0xbfb8aa3b, v44
	v_add_f32_e32 v48, 1.0, v48
	v_add_f32_e32 v34, 1.0, v60
	v_add_f32_e32 v35, 1.0, v35
	v_rcp_f32_e32 v48, v48
	v_rcp_f32_e32 v34, v34
	v_rcp_f32_e32 v35, v35
	v_add_f32_e32 v56, 0x3b886211, v54
	v_exp_f32_e32 v44, v44
	v_fmac_f32_e32 v56, -2.0, v48
	v_pk_fma_f32 v[34:35], v[34:35], -2.0, v[128:129] op_sel_hi:[1,0,1]
	v_mul_f32_e32 v126, v56, v56
	v_fmac_f32_e32 v126, v35, v35
	v_cndmask_b32_e32 v46, 0, v46, vcc
	v_add_f32_e32 v48, v34, v35
	v_fmac_f32_e32 v126, v34, v34
	v_add_f32_e32 v34, 1.0, v44
	v_cmp_eq_u32_e32 vcc, 1, v28
	v_add_f32_e32 v60, v48, v56
	v_rcp_f32_e32 v44, v34
	v_mul_f32_e32 v34, v36, v36
	v_cndmask_b32_e64 v35, 0, 1.0, vcc
	v_add_f32_e32 v47, v35, v47
	v_cndmask_b32_e32 v35, 0, v34, vcc
	v_cndmask_b32_e32 v48, 0, v36, vcc
	v_cndmask_b32_e32 v56, 0, v60, vcc
	v_cmp_eq_u32_e32 vcc, 2, v28
	v_add_f32_e32 v55, v35, v55
	v_add_f32_e32 v56, v127, v56
	v_cndmask_b32_e64 v35, 0, 1.0, vcc
	v_add_f32_e32 v48, v48, v74
	v_add_f32_e32 v74, v35, v135
	v_cndmask_b32_e32 v35, 0, v34, vcc
	v_cndmask_b32_e32 v127, 0, v36, vcc
	v_cndmask_b32_e32 v135, 0, v60, vcc
	v_cmp_eq_u32_e32 vcc, 3, v28
	v_add_f32_e32 v140, v140, v145
	v_add_f32_e32 v139, v35, v139
	v_cndmask_b32_e64 v35, 0, 1.0, vcc
	v_add_f32_e32 v135, v140, v135
	v_add_f32_e32 v140, v35, v141
	v_mul_f32_e32 v35, 0x4038aa3b, v61
	v_exp_f32_e32 v35, v35
	v_add_f32_e32 v138, v127, v138
	v_cndmask_b32_e32 v127, 0, v34, vcc
	v_cndmask_b32_e32 v34, 0, v36, vcc
	v_add_f32_e32 v141, v34, v143
	v_add_f32_e32 v34, 1.0, v35
	v_mul_f32_e32 v35, 0x4038aa3b, v49
	v_mul_f32_e32 v49, 0x4038aa3b, v57
	v_exp_f32_e32 v49, v49
	v_exp_f32_e32 v35, v35
	v_rcp_f32_e32 v34, v34
	v_mul_f32_e32 v45, 0xbfb8aa3b, v45
	v_add_f32_e32 v49, 1.0, v49
	v_add_f32_e32 v35, 1.0, v35
	v_rcp_f32_e32 v49, v49
	v_rcp_f32_e32 v35, v35
	v_add_f32_e32 v54, 0x3bcc931a, v54
	v_exp_f32_e32 v45, v45
	v_mul_f32_e32 v42, 0xbfb8aa3b, v42
	v_mul_f32_e32 v43, 0xbfb8aa3b, v43
	v_add_f32_e32 v46, v46, v144
	v_fmac_f32_e32 v54, -2.0, v49
	v_exp_f32_e32 v42, v42
	v_exp_f32_e32 v43, v43
	v_add_f32_e32 v46, v127, v46
	v_pk_fma_f32 v[34:35], v[34:35], -2.0, v[128:129] op_sel_hi:[1,0,1]
	v_mul_f32_e32 v127, v54, v54
	v_fmac_f32_e32 v127, v35, v35
	v_cndmask_b32_e32 v36, 0, v60, vcc
	v_add_f32_e32 v49, v34, v35
	v_fmac_f32_e32 v127, v34, v34
	v_add_f32_e32 v34, 1.0, v45
	v_cmp_eq_u32_e32 vcc, 1, v29
	v_add_f32_e32 v61, v49, v54
	v_rcp_f32_e32 v45, v34
	v_mul_f32_e32 v34, v37, v37
	v_cndmask_b32_e64 v35, 0, 1.0, vcc
	v_add_f32_e32 v42, 1.0, v42
	v_add_f32_e32 v43, 1.0, v43
	v_add_f32_e32 v47, v35, v47
	v_cndmask_b32_e32 v35, 0, v34, vcc
	v_cndmask_b32_e32 v49, 0, v37, vcc
	v_cndmask_b32_e32 v54, 0, v61, vcc
	v_cmp_eq_u32_e32 vcc, 2, v29
	v_rcp_f32_e32 v42, v42
	v_rcp_f32_e32 v43, v43
	v_add_f32_e32 v48, v49, v48
	v_add_f32_e32 v49, v35, v55
	v_cndmask_b32_e64 v35, 0, 1.0, vcc
	v_add_f32_e32 v54, v56, v54
	v_add_f32_e32 v55, v35, v74
	v_cndmask_b32_e32 v35, 0, v34, vcc
	v_cndmask_b32_e32 v56, 0, v37, vcc
	v_cndmask_b32_e32 v57, 0, v61, vcc
	v_cmp_eq_u32_e32 vcc, 3, v29
	v_add_f32_e32 v74, v35, v139
	v_add_f32_e32 v36, v142, v36
	v_cndmask_b32_e64 v35, 0, 1.0, vcc
	v_cndmask_b32_e32 v34, 0, v34, vcc
	v_add_f32_e32 v57, v135, v57
	v_add_f32_e32 v56, v56, v138
	v_add_f32_e32 v138, v35, v140
	v_cndmask_b32_e32 v35, 0, v37, vcc
	v_cndmask_b32_e32 v37, 0, v61, vcc
	v_add_f32_e32 v46, v34, v46
	v_add_u32_e32 v135, 0x1e000, v134
	v_add_f32_e32 v36, v36, v37
	v_add_f32_e32 v37, v35, v141
	ds_write_b128 v135, v[42:45]
	v_add_u32_e32 v34, 0x1500, v137
	s_waitcnt vmcnt(5)
	v_mul_f32_e32 v43, 0x4038aa3b, v70
	v_mul_u32_u24_sdwa v35, v34, s6 dst_sel:DWORD dst_unused:UNUSED_PAD src0_sel:WORD_0 src1_sel:DWORD
	v_exp_f32_e32 v43, v43
	v_lshrrev_b32_e32 v35, 23, v35
	v_mul_i32_i24_e32 v42, 0xffffff60, v35
	v_cvt_f32_u32_e32 v44, v35
	v_add_lshl_u32 v34, v42, v34, 2
	s_waitcnt vmcnt(4)
	v_mul_f32_e32 v35, 0x4038aa3b, v62
	v_cvt_f32_i32_e32 v42, v34
	v_add_f32_e32 v34, 1.0, v43
	v_exp_f32_e32 v35, v35
	s_waitcnt vmcnt(3)
	v_mul_f32_e32 v43, 0x4038aa3b, v66
	v_exp_f32_e32 v43, v43
	v_rcp_f32_e32 v34, v34
	v_add_f32_e32 v35, 1.0, v35
	v_rcp_f32_e32 v35, v35
	v_add_f32_e32 v43, 1.0, v43
	v_rcp_f32_e32 v43, v43
	v_fma_f32 v129, v44, s7, 1.0
	v_fma_f32 v42, v42, s9, 1.0
	v_pk_fma_f32 v[34:35], v[34:35], -2.0, v[128:129] op_sel_hi:[1,0,1]
	v_fma_f32 v43, -2.0, v43, v42
	v_add_f32_e32 v44, v34, v35
	v_add_f32_e32 v62, v44, v43
	s_waitcnt vmcnt(1)
	v_mul_f32_e32 v44, 0xbfb8aa3b, v50
	v_exp_f32_e32 v44, v44
	v_mul_f32_e32 v66, v43, v43
	s_waitcnt vmcnt(0)
	v_cmp_eq_u32_e32 vcc, 1, v30
	v_fmac_f32_e32 v66, v35, v35
	v_mul_f32_e32 v35, v38, v38
	v_cndmask_b32_e64 v43, 0, 1.0, vcc
	v_fmac_f32_e32 v66, v34, v34
	v_add_f32_e32 v34, 1.0, v44
	v_add_f32_e32 v43, v47, v43
	v_cndmask_b32_e32 v44, 0, v35, vcc
	v_cndmask_b32_e32 v45, 0, v38, vcc
	v_cndmask_b32_e32 v47, 0, v62, vcc
	v_cmp_eq_u32_e32 vcc, 2, v30
	v_add_f32_e32 v47, v54, v47
	v_add_f32_e32 v45, v48, v45
	v_cndmask_b32_e32 v50, 0, v38, vcc
	v_add_f32_e32 v50, v56, v50
	v_mul_f32_e32 v56, 0x4038aa3b, v71
	v_exp_f32_e32 v56, v56
	v_add_f32_e32 v44, v49, v44
	v_cndmask_b32_e64 v48, 0, 1.0, vcc
	v_cndmask_b32_e32 v49, 0, v35, vcc
	v_cndmask_b32_e32 v54, 0, v62, vcc
	v_cmp_eq_u32_e32 vcc, 3, v30
	v_add_f32_e32 v54, v57, v54
	v_mul_f32_e32 v51, 0xbfb8aa3b, v51
	v_cndmask_b32_e32 v57, 0, v62, vcc
	v_cndmask_b32_e32 v38, 0, v38, vcc
	v_add_f32_e32 v57, v36, v57
	v_add_f32_e32 v36, 1.0, v56
	v_mul_f32_e32 v56, 0x4038aa3b, v67
	v_add_f32_e32 v38, v37, v38
	v_mul_f32_e32 v37, 0x4038aa3b, v63
	v_exp_f32_e32 v56, v56
	v_exp_f32_e32 v37, v37
	v_rcp_f32_e32 v36, v36
	v_cndmask_b32_e32 v35, 0, v35, vcc
	v_add_f32_e32 v56, 1.0, v56
	v_add_f32_e32 v37, 1.0, v37
	v_rcp_f32_e32 v56, v56
	v_rcp_f32_e32 v37, v37
	v_add_f32_e32 v46, v46, v35
	v_add_f32_e32 v35, 0x3b086211, v42
	v_fmac_f32_e32 v35, -2.0, v56
	v_exp_f32_e32 v51, v51
	v_pk_fma_f32 v[36:37], v[36:37], -2.0, v[128:129] op_sel_hi:[1,0,1]
	v_mul_f32_e32 v67, v35, v35
	v_add_f32_e32 v48, v55, v48
	v_cndmask_b32_e64 v55, 0, 1.0, vcc
	v_add_f32_e32 v56, v36, v37
	v_fmac_f32_e32 v67, v37, v37
	v_cmp_eq_u32_e32 vcc, 1, v31
	v_add_f32_e32 v63, v56, v35
	v_fmac_f32_e32 v67, v36, v36
	v_mul_f32_e32 v36, v39, v39
	v_cndmask_b32_e64 v37, 0, 1.0, vcc
	v_add_f32_e32 v35, 1.0, v51
	v_add_f32_e32 v43, v37, v43
	v_cndmask_b32_e32 v37, 0, v36, vcc
	v_cndmask_b32_e32 v51, 0, v39, vcc
	v_cndmask_b32_e32 v56, 0, v63, vcc
	v_cmp_eq_u32_e32 vcc, 2, v31
	v_add_f32_e32 v44, v37, v44
	v_add_f32_e32 v49, v74, v49
	v_cndmask_b32_e64 v37, 0, 1.0, vcc
	v_add_f32_e32 v47, v47, v56
	v_add_f32_e32 v45, v51, v45
	v_add_f32_e32 v48, v37, v48
	v_cndmask_b32_e32 v37, 0, v36, vcc
	v_cndmask_b32_e32 v51, 0, v39, vcc
	v_cndmask_b32_e32 v56, 0, v63, vcc
	v_cmp_eq_u32_e32 vcc, 3, v31
	v_add_f32_e32 v55, v138, v55
	v_add_f32_e32 v49, v37, v49
	v_cndmask_b32_e64 v37, 0, 1.0, vcc
	v_add_f32_e32 v50, v51, v50
	v_add_f32_e32 v51, v37, v55
	v_mul_f32_e32 v37, 0x4038aa3b, v72
	v_exp_f32_e32 v37, v37
	v_add_f32_e32 v54, v54, v56
	v_cndmask_b32_e32 v55, 0, v36, vcc
	v_cndmask_b32_e32 v36, 0, v39, vcc
	v_mul_f32_e32 v56, 0x4038aa3b, v68
	v_add_f32_e32 v38, v36, v38
	v_add_f32_e32 v36, 1.0, v37
	v_mul_f32_e32 v37, 0x4038aa3b, v64
	v_exp_f32_e32 v56, v56
	v_exp_f32_e32 v37, v37
	v_rcp_f32_e32 v36, v36
	v_mul_f32_e32 v52, 0xbfb8aa3b, v52
	v_add_f32_e32 v56, 1.0, v56
	v_add_f32_e32 v37, 1.0, v37
	v_rcp_f32_e32 v56, v56
	v_rcp_f32_e32 v37, v37
	v_add_f32_e32 v46, v55, v46
	v_add_f32_e32 v55, 0x3b886211, v42
	v_exp_f32_e32 v52, v52
	v_fmac_f32_e32 v55, -2.0, v56
	v_pk_fma_f32 v[36:37], v[36:37], -2.0, v[128:129] op_sel_hi:[1,0,1]
	v_mul_f32_e32 v68, v55, v55
	v_cndmask_b32_e32 v39, 0, v63, vcc
	v_add_f32_e32 v56, v36, v37
	v_fmac_f32_e32 v68, v37, v37
	v_cmp_eq_u32_e32 vcc, 1, v32
	v_add_f32_e32 v64, v56, v55
	v_fmac_f32_e32 v68, v36, v36
	v_add_f32_e32 v36, 1.0, v52
	v_mul_f32_e32 v37, v40, v40
	v_cndmask_b32_e64 v52, 0, 1.0, vcc
	v_add_f32_e32 v43, v52, v43
	v_cndmask_b32_e32 v52, 0, v37, vcc
	v_cndmask_b32_e32 v55, 0, v40, vcc
	v_cndmask_b32_e32 v56, 0, v64, vcc
	v_cmp_eq_u32_e32 vcc, 2, v32
	v_add_f32_e32 v44, v52, v44
	v_add_f32_e32 v47, v47, v56
	v_cndmask_b32_e64 v52, 0, 1.0, vcc
	v_add_f32_e32 v45, v55, v45
	v_add_f32_e32 v48, v52, v48
	v_cndmask_b32_e32 v52, 0, v37, vcc
	v_cndmask_b32_e32 v55, 0, v40, vcc
	v_cndmask_b32_e32 v56, 0, v64, vcc
	v_cmp_eq_u32_e32 vcc, 3, v32
	v_add_f32_e32 v49, v52, v49
	v_add_f32_e32 v39, v57, v39
	v_cndmask_b32_e64 v52, 0, 1.0, vcc
	v_add_f32_e32 v51, v52, v51
	v_mul_f32_e32 v52, 0x4038aa3b, v73
	v_exp_f32_e32 v52, v52
	v_add_f32_e32 v50, v55, v50
	v_cndmask_b32_e32 v55, 0, v64, vcc
	v_cndmask_b32_e32 v40, 0, v40, vcc
	v_add_f32_e32 v55, v39, v55
	v_mul_f32_e32 v39, 0x4038aa3b, v65
	v_add_f32_e32 v40, v40, v38
	v_add_f32_e32 v38, 1.0, v52
	v_exp_f32_e32 v39, v39
	v_mul_f32_e32 v52, 0x4038aa3b, v69
	v_exp_f32_e32 v52, v52
	v_rcp_f32_e32 v38, v38
	v_add_f32_e32 v39, 1.0, v39
	v_rcp_f32_e32 v39, v39
	v_add_f32_e32 v52, 1.0, v52
	v_rcp_f32_e32 v52, v52
	v_cndmask_b32_e32 v37, 0, v37, vcc
	v_add_f32_e32 v46, v37, v46
	v_add_f32_e32 v37, 0x3bcc931a, v42
	v_pk_fma_f32 v[38:39], v[38:39], -2.0, v[128:129] op_sel_hi:[1,0,1]
	v_fmac_f32_e32 v37, -2.0, v52
	v_add_f32_e32 v42, v38, v39
	v_add_f32_e32 v65, v42, v37
	v_mul_f32_e32 v42, 0xbfb8aa3b, v53
	v_exp_f32_e32 v42, v42
	v_mul_f32_e32 v69, v37, v37
	v_fmac_f32_e32 v69, v39, v39
	v_cmp_eq_u32_e32 vcc, 1, v33
	v_fmac_f32_e32 v69, v38, v38
	v_mul_f32_e32 v38, v41, v41
	v_cndmask_b32_e64 v39, 0, 1.0, vcc
	v_add_f32_e32 v37, 1.0, v42
	v_add_f32_e32 v145, v39, v43
	v_cndmask_b32_e32 v39, 0, v38, vcc
	v_cndmask_b32_e32 v42, 0, v41, vcc
	v_cndmask_b32_e32 v43, 0, v65, vcc
	v_cmp_eq_u32_e32 vcc, 2, v33
	v_add_f32_e32 v142, v39, v44
	v_rcp_f32_e32 v34, v34
	v_cndmask_b32_e64 v39, 0, 1.0, vcc
	v_rcp_f32_e32 v35, v35
	v_rcp_f32_e32 v36, v36
	v_rcp_f32_e32 v37, v37
	v_add_f32_e32 v143, v47, v43
	v_add_f32_e32 v144, v42, v45
	v_add_f32_e32 v141, v39, v48
	v_cndmask_b32_e32 v39, 0, v38, vcc
	v_cndmask_b32_e32 v42, 0, v41, vcc
	v_cndmask_b32_e32 v43, 0, v65, vcc
	v_cmp_eq_u32_e32 vcc, 3, v33
	v_add_f32_e32 v138, v39, v49
	v_add_f32_e32 v54, v54, v56
	v_cndmask_b32_e64 v39, 0, 1.0, vcc
	v_add_f32_e32 v137, v39, v51
	v_cndmask_b32_e32 v38, 0, v38, vcc
	v_cndmask_b32_e32 v39, 0, v41, vcc
	v_cndmask_b32_e32 v41, 0, v65, vcc
	v_add_f32_e32 v139, v54, v43
	v_add_f32_e32 v140, v42, v50
	v_add_f32_e32 v72, v55, v41
	v_add_f32_e32 v73, v39, v40
	v_add_f32_e32 v71, v38, v46
	v_add_u32_e32 v70, 0x21000, v134
	ds_write_b128 v70, v[34:37]
	v_mov_b32_e32 v74, v75
	v_mov_b32_e32 v51, v75
	v_mov_b32_e32 v50, v75
	v_mov_b32_e32 v47, v75
	v_mov_b32_e32 v46, v75
	v_mov_b32_e32 v55, v75
	v_mov_b32_e32 v54, v75
	v_mov_b32_e32 v40, v75
	s_and_saveexec_b64 s[10:11], s[4:5]
	s_cbranch_execz .LBB0_2
	s_mov_b64 s[12:13], 0xc80000
	v_lshl_add_u64 v[34:35], v[130:131], 0, s[12:13]
	s_mov_b64 s[12:13], 0x1900000
	v_lshl_add_u64 v[36:37], v[130:131], 0, s[12:13]
	s_mov_b64 s[12:13], 0x2580000
	v_lshl_add_u64 v[38:39], v[130:131], 0, s[12:13]
	s_mov_b64 s[12:13], 0x3200000
	v_lshl_add_u64 v[42:43], v[130:131], 0, s[12:13]
	s_movk_i32 s12, 0xff
	v_mov_b32_e32 v40, 0x18000
	v_cmp_lt_u32_e32 vcc, s12, v0
	v_mov_b32_e32 v75, 0
	s_nop 0
	v_cndmask_b32_e64 v74, v40, 0, vcc
	v_lshl_add_u64 v[40:41], v[130:131], 0, v[74:75]
	v_lshl_add_u64 v[34:35], v[34:35], 0, v[74:75]
	global_load_dwordx4 v[54:57], v[40:41], off sc0 nt
	global_load_dwordx4 v[50:53], v[34:35], off sc0 nt
	v_lshl_add_u64 v[34:35], v[36:37], 0, v[74:75]
	v_lshl_add_u64 v[36:37], v[38:39], 0, v[74:75]
	global_load_dwordx4 v[46:49], v[34:35], off sc0 nt
	global_load_dwordx4 v[38:41], v[36:37], off sc0 nt
	v_lshl_add_u64 v[34:35], v[42:43], 0, v[74:75]
	global_load_dwordx4 v[42:45], v[34:35], off sc0 nt
	v_lshl_add_u64 v[34:35], v[132:133], 0, v[74:75]
	global_load_dwordx4 v[34:37], v[34:35], off sc0 nt
	v_or_b32_e32 v130, 0x1800, v0
	v_add_u32_e32 v74, s8, v130
	v_mul_u32_u24_sdwa v75, v74, s6 dst_sel:DWORD dst_unused:UNUSED_PAD src0_sel:WORD_0 src1_sel:DWORD
	v_lshrrev_b32_e32 v75, 23, v75
	v_mul_i32_i24_e32 v129, 0xffffff60, v75
	v_add_lshl_u32 v74, v129, v74, 2
	v_cvt_f32_u32_e32 v75, v75
	v_cvt_f32_i32_e32 v74, v74
	v_fma_f32 v129, v75, s7, 1.0
	v_fma_f32 v131, v74, s9, 1.0
	s_waitcnt vmcnt(5)
	v_mul_f32_e32 v54, 0x4038aa3b, v54
	s_waitcnt vmcnt(4)
	v_mul_f32_e32 v50, 0x4038aa3b, v50
	v_exp_f32_e32 v54, v54
	s_waitcnt vmcnt(3)
	v_mul_f32_e32 v46, 0x4038aa3b, v46
	v_exp_f32_e32 v50, v50
	v_exp_f32_e32 v46, v46
	v_mul_f32_e32 v47, 0x4038aa3b, v47
	v_mul_f32_e32 v55, 0x4038aa3b, v55
	v_exp_f32_e32 v148, v47
	v_add_f32_e32 v47, 1.0, v54
	v_add_f32_e32 v50, 1.0, v50
	v_add_f32_e32 v54, 1.0, v46
	v_exp_f32_e32 v55, v55
	v_rcp_f32_e32 v46, v47
	v_rcp_f32_e32 v47, v50
	v_rcp_f32_e32 v50, v54
	v_mul_f32_e32 v51, 0x4038aa3b, v51
	s_waitcnt vmcnt(0)
	v_cmp_eq_u32_e32 vcc, 1, v34
	v_cmp_eq_u32_e64 s[6:7], 2, v34
	v_cmp_eq_u32_e64 s[8:9], 3, v34
	v_exp_f32_e32 v51, v51
	v_mul_f32_e32 v74, v38, v38
	v_cndmask_b32_e64 v75, 0, 1.0, vcc
	v_cndmask_b32_e64 v132, 0, 1.0, s[6:7]
	v_cndmask_b32_e64 v133, 0, 1.0, s[8:9]
	v_add_f32_e32 v55, 1.0, v55
	v_pk_fma_f32 v[46:47], v[46:47], -2.0, v[128:129] op_sel_hi:[1,0,1]
	v_fma_f32 v54, -2.0, v50, v131
	v_add_f32_e32 v145, v145, v75
	v_cndmask_b32_e32 v75, 0, v74, vcc
	v_add_f32_e32 v132, v141, v132
	v_cndmask_b32_e64 v141, 0, v74, s[6:7]
	v_add_f32_e32 v133, v137, v133
	v_cndmask_b32_e64 v137, 0, v74, s[8:9]
	v_rcp_f32_e32 v74, v55
	v_add_f32_e32 v55, v46, v47
	v_mul_f32_e32 v50, v54, v54
	v_add_f32_e32 v54, v55, v54
	v_fmac_f32_e32 v50, v47, v47
	v_cndmask_b32_e32 v146, 0, v38, vcc
	v_cndmask_b32_e64 v147, 0, v38, s[6:7]
	v_cndmask_b32_e64 v38, 0, v38, s[8:9]
	v_add_f32_e32 v51, 1.0, v51
	v_fmac_f32_e32 v50, v46, v46
	v_cndmask_b32_e32 v46, 0, v54, vcc
	v_add_f32_e32 v142, v142, v75
	v_add_f32_e32 v38, v73, v38
	v_add_f32_e32 v73, v143, v46
	v_rcp_f32_e32 v75, v51
	v_add_f32_e32 v46, 1.0, v148
	v_rcp_f32_e32 v51, v46
	v_cndmask_b32_e64 v47, 0, v54, s[6:7]
	v_add_f32_e32 v139, v139, v47
	v_add_f32_e32 v71, v71, v137
	v_add_f32_e32 v137, 0x3b086211, v131
	v_pk_fma_f32 v[46:47], v[74:75], -2.0, v[128:129] op_sel_hi:[1,0,1]
	v_cndmask_b32_e64 v55, 0, v54, s[8:9]
	v_fmac_f32_e32 v137, -2.0, v51
	v_add_f32_e32 v51, v46, v47
	v_add_f32_e32 v72, v72, v55
	v_add_f32_e32 v55, v51, v137
	v_mul_f32_e32 v51, v137, v137
	v_fmac_f32_e32 v51, v47, v47
	v_fmac_f32_e32 v51, v46, v46
	v_mul_f32_e32 v46, v39, v39
	v_cmp_eq_u32_e32 vcc, 1, v35
	v_add_f32_e32 v138, v138, v141
	v_add_f32_e32 v140, v140, v147
	v_cndmask_b32_e64 v47, 0, 1.0, vcc
	v_cndmask_b32_e32 v74, 0, v46, vcc
	v_cndmask_b32_e32 v75, 0, v39, vcc
	v_cndmask_b32_e32 v137, 0, v55, vcc
	v_cmp_eq_u32_e32 vcc, 2, v35
	v_add_f32_e32 v73, v73, v137
	v_add_f32_e32 v137, v74, v142
	v_cndmask_b32_e64 v74, 0, 1.0, vcc
	v_add_f32_e32 v132, v74, v132
	v_cndmask_b32_e32 v74, 0, v46, vcc
	v_cndmask_b32_e32 v141, 0, v39, vcc
	v_cndmask_b32_e32 v142, 0, v55, vcc
	v_cmp_eq_u32_e32 vcc, 3, v35
	v_mul_f32_e32 v48, 0x4038aa3b, v48
	v_add_f32_e32 v140, v141, v140
	v_cndmask_b32_e32 v39, 0, v39, vcc
	v_mul_f32_e32 v56, 0x4038aa3b, v56
	v_add_f32_e32 v141, v39, v38
	v_mul_f32_e32 v39, 0x4038aa3b, v52
	v_exp_f32_e32 v48, v48
	v_exp_f32_e32 v56, v56
	v_exp_f32_e32 v39, v39
	v_mul_f32_e32 v44, 0xbfb8aa3b, v44
	v_add_f32_e32 v48, 1.0, v48
	v_add_f32_e32 v38, 1.0, v56
	v_add_f32_e32 v39, 1.0, v39
	v_rcp_f32_e32 v48, v48
	v_rcp_f32_e32 v38, v38
	v_rcp_f32_e32 v39, v39
	v_add_f32_e32 v138, v74, v138
	v_cndmask_b32_e64 v74, 0, 1.0, vcc
	v_add_f32_e32 v56, 0x3b886211, v131
	v_exp_f32_e32 v44, v44
	v_add_f32_e32 v133, v74, v133
	v_cndmask_b32_e32 v74, 0, v55, vcc
	v_fmac_f32_e32 v56, -2.0, v48
	v_add_f32_e32 v72, v72, v74
	v_pk_fma_f32 v[38:39], v[38:39], -2.0, v[128:129] op_sel_hi:[1,0,1]
	v_mul_f32_e32 v74, v56, v56
	v_cndmask_b32_e32 v46, 0, v46, vcc
	v_fmac_f32_e32 v74, v39, v39
	v_add_f32_e32 v52, v46, v71
	v_add_f32_e32 v46, v38, v39
	v_fmac_f32_e32 v74, v38, v38
	v_add_f32_e32 v38, 1.0, v44
	v_cmp_eq_u32_e32 vcc, 1, v36
	v_add_f32_e32 v47, v47, v145
	v_add_f32_e32 v46, v46, v56
	v_rcp_f32_e32 v44, v38
	v_mul_f32_e32 v38, v40, v40
	v_cndmask_b32_e64 v39, 0, 1.0, vcc
	v_add_f32_e32 v144, v144, v146
	v_add_f32_e32 v48, v39, v47
	v_cndmask_b32_e32 v39, 0, v38, vcc
	v_cndmask_b32_e32 v47, 0, v40, vcc
	v_cndmask_b32_e32 v56, 0, v46, vcc
	v_cmp_eq_u32_e32 vcc, 2, v36
	v_add_f32_e32 v75, v75, v144
	v_add_f32_e32 v56, v73, v56
	v_add_f32_e32 v73, v39, v137
	v_cndmask_b32_e64 v39, 0, 1.0, vcc
	v_add_f32_e32 v71, v47, v75
	v_add_f32_e32 v132, v39, v132
	v_cndmask_b32_e32 v39, 0, v38, vcc
	v_cndmask_b32_e32 v47, 0, v40, vcc
	v_cndmask_b32_e32 v75, 0, v46, vcc
	v_cmp_eq_u32_e32 vcc, 3, v36
	v_add_f32_e32 v138, v39, v138
	v_add_f32_e32 v140, v47, v140
	v_cndmask_b32_e64 v39, 0, 1.0, vcc
	v_add_f32_e32 v133, v39, v133
	v_mul_f32_e32 v39, 0x4038aa3b, v57
	v_exp_f32_e32 v39, v39
	v_cndmask_b32_e32 v47, 0, v38, vcc
	v_cndmask_b32_e32 v38, 0, v40, vcc
	v_mul_f32_e32 v49, 0x4038aa3b, v49
	v_add_f32_e32 v57, v38, v141
	v_add_f32_e32 v38, 1.0, v39
	v_mul_f32_e32 v39, 0x4038aa3b, v53
	v_exp_f32_e32 v49, v49
	v_exp_f32_e32 v39, v39
	v_rcp_f32_e32 v38, v38
	v_mul_f32_e32 v45, 0xbfb8aa3b, v45
	v_add_f32_e32 v49, 1.0, v49
	v_add_f32_e32 v39, 1.0, v39
	v_rcp_f32_e32 v49, v49
	v_rcp_f32_e32 v39, v39
	v_add_f32_e32 v53, 0x3bcc931a, v131
	v_exp_f32_e32 v45, v45
	v_add_f32_e32 v139, v139, v142
	v_fmac_f32_e32 v53, -2.0, v49
	v_mul_f32_e32 v42, 0xbfb8aa3b, v42
	v_mul_f32_e32 v43, 0xbfb8aa3b, v43
	v_add_f32_e32 v137, v139, v75
	v_pk_fma_f32 v[38:39], v[38:39], -2.0, v[128:129] op_sel_hi:[1,0,1]
	v_mul_f32_e32 v75, v53, v53
	v_exp_f32_e32 v42, v42
	v_exp_f32_e32 v43, v43
	v_fmac_f32_e32 v75, v39, v39
	v_cndmask_b32_e32 v40, 0, v46, vcc
	v_add_f32_e32 v52, v47, v52
	v_add_f32_e32 v47, v38, v39
	v_fmac_f32_e32 v75, v38, v38
	v_add_f32_e32 v38, 1.0, v45
	v_cmp_eq_u32_e32 vcc, 1, v37
	v_add_f32_e32 v47, v47, v53
	v_rcp_f32_e32 v45, v38
	v_mul_f32_e32 v38, v41, v41
	v_cndmask_b32_e64 v39, 0, 1.0, vcc
	v_add_f32_e32 v145, v39, v48
	v_cndmask_b32_e32 v39, 0, v38, vcc
	v_cndmask_b32_e32 v48, 0, v41, vcc
	v_cndmask_b32_e32 v49, 0, v47, vcc
	v_cmp_eq_u32_e32 vcc, 2, v37
	v_add_f32_e32 v42, 1.0, v42
	v_add_f32_e32 v43, 1.0, v43
	v_add_f32_e32 v142, v39, v73
	v_cndmask_b32_e64 v39, 0, 1.0, vcc
	v_rcp_f32_e32 v42, v42
	v_rcp_f32_e32 v43, v43
	v_add_f32_e32 v143, v56, v49
	v_add_f32_e32 v144, v48, v71
	v_add_f32_e32 v141, v39, v132
	v_cndmask_b32_e32 v39, 0, v38, vcc
	v_cndmask_b32_e32 v48, 0, v41, vcc
	v_cndmask_b32_e32 v49, 0, v47, vcc
	v_cmp_eq_u32_e32 vcc, 3, v37
	v_add_f32_e32 v138, v39, v138
	v_lshlrev_b32_e32 v36, 16, v36
	v_cndmask_b32_e64 v39, 0, 1.0, vcc
	v_add_f32_e32 v40, v72, v40
	v_add_f32_e32 v139, v137, v49
	v_add_f32_e32 v137, v39, v133
	v_cndmask_b32_e32 v38, 0, v38, vcc
	v_cndmask_b32_e32 v39, 0, v41, vcc
	v_cndmask_b32_e32 v41, 0, v47, vcc
	v_lshlrev_b32_e32 v37, 24, v37
	v_lshl_or_b32 v35, v35, 8, v36
	v_add_f32_e32 v140, v48, v140
	v_add_f32_e32 v72, v40, v41
	v_add_f32_e32 v73, v39, v57
	v_add_f32_e32 v71, v38, v52
	v_lshl_add_u32 v38, v130, 4, v136
	v_or3_b32 v40, v35, v37, v34
	ds_write_b128 v38, v[42:45] offset:49152
